# attention softmax reductions by permlane16/32 swap instead of ds_bpermute; next token's score row requested after the attention steps
# baseline (speedup 1.0000x reference)
.LBB0_516:
	s_cmp_lt_i32 s44, 5
	s_cselect_b64 s[2:3], -1, 0
	s_add_u32 s70, s54, 0x20c00000
	s_addc_u32 s71, s55, 0
	s_add_u32 s4, s54, 0x1800000
	s_addc_u32 s5, s55, 0
	s_and_b64 s[20:21], s[2:3], s[0:1]
	v_writelane_b32 v242, s4, 39
	s_andn2_b64 vcc, exec, s[20:21]
	s_nop 0
	v_writelane_b32 v242, s5, 40
	s_cbranch_vccnz .LBB0_1160
	s_lshl_b32 s0, s77, 3
	s_add_i32 s22, s76, s0
	s_lshl_b32 s40, s97, 3
	s_cmpk_lt_i32 s22, 0x2000
	v_mbcnt_hi_u32_b32 v1, -1, v175
	s_cselect_b64 s[0:1], -1, 0
	s_mov_b32 s91, 0
	s_waitcnt vmcnt(1)
	v_mov_b32_e32 v78, v1
	s_movk_i32 s41, 0x2000
	v_writelane_b32 v242, s0, 41
	s_cmpk_gt_i32 s22, 0x1fff
	v_and_b32_e32 v159, 64, v1
	v_xor_b32_e32 v155, 16, v1
	v_xor_b32_e32 v154, 32, v1
	v_xor_b32_e32 v160, 1, v1
	v_xor_b32_e32 v158, 2, v1
	v_xor_b32_e32 v157, 4, v1
	v_xor_b32_e32 v156, 8, v1
	v_writelane_b32 v242, s1, 42
	s_cbranch_scc1 .LBB0_1141
	v_writelane_b32 v242, s20, 43
	s_mov_b32 s98, 0
	s_mul_i32 s0, s76, 0x2800
	s_add_i32 s89, s0, 0
	v_writelane_b32 v242, s21, 44
	v_writelane_b32 v242, s96, 45
	v_writelane_b32 v242, s78, 46
	v_add_u32_e32 v2, 64, v159
	s_mov_b32 s0, s22
	v_writelane_b32 v242, s79, 47
	v_writelane_b32 v242, s77, 48
	v_writelane_b32 v242, s76, 49
	v_writelane_b32 v242, s97, 50
	v_cmp_lt_i32_e32 vcc, v155, v2
	v_writelane_b32 v242, s0, 51
	s_lshl_b32 s12, s97, 4
	v_cndmask_b32_e32 v3, v1, v155, vcc
	v_cmp_lt_i32_e32 vcc, v154, v2
	v_writelane_b32 v242, s1, 52
	v_lshlrev_b32_e32 v161, 2, v3
	v_cndmask_b32_e32 v3, v1, v154, vcc
	v_cmp_lt_i32_e32 vcc, v160, v2
	v_writelane_b32 v242, s82, 53
	v_lshlrev_b32_e32 v162, 2, v3
	v_cndmask_b32_e32 v3, v1, v160, vcc
	v_cmp_lt_i32_e32 vcc, v158, v2
	v_writelane_b32 v242, s83, 54
	v_lshlrev_b32_e32 v163, 2, v3
	v_cndmask_b32_e32 v3, v1, v158, vcc
	v_cmp_lt_i32_e32 vcc, v157, v2
	v_writelane_b32 v242, s84, 55
	v_lshlrev_b32_e32 v164, 2, v3
	v_cndmask_b32_e32 v3, v1, v157, vcc
	v_cmp_lt_i32_e32 vcc, v156, v2
	v_writelane_b32 v242, s85, 56
	v_writelane_b32 v242, s86, 57
	v_cndmask_b32_e32 v2, v1, v156, vcc
	v_lshlrev_b32_e32 v165, 2, v3
	v_lshlrev_b32_e32 v166, 2, v2
	s_movk_i32 s33, 0x1000
	s_movk_i32 s56, 0x3000
	s_mov_b32 s64, 0x7060302
	s_mov_b32 s65, 0x10001
	v_mov_b32_e32 v147, 0
	v_mov_b32_e32 v167, 0x10001
	s_mov_b32 s34, 0x5040100
	s_movk_i32 s35, 0x3400
	s_mov_b64 s[94:95], 0x2800
	s_mov_b32 s13, 0x42fe0000
	s_mov_b32 s57, 0x40c0c00
	s_mov_b32 s88, 0xf800000
	v_mov_b32_e32 v168, 0x260
	v_bfrev_b32_e32 v169, 1
	v_mov_b32_e32 v170, 0xff800000
	v_mov_b32_e32 v171, 0x80
	s_mov_b32 s42, s22
	s_mov_b32 s14, 0
	s_mov_b32 s43, s22
	v_writelane_b32 v242, s87, 58
	v_writelane_b32 v242, s12, 59
	s_branch .LBB0_520

.LBB0_520:
	s_lshr_b32 s0, s43, 2
	s_lshr_b32 s1, s43, 11
	s_xor_b32 s0, s1, s0
	s_xor_b32 s0, s0, s43
	s_bfe_u32 s1, s43, 0xb0001
	s_and_b32 s0, s0, 1
	s_xor_b32 s2, s1, 0xfff
	s_cmp_eq_u32 s0, 0
	s_cselect_b32 s90, s1, s2
	s_ashr_i32 s78, s43, 12
	s_ashr_i32 s79, s78, 31
	s_lshl_b64 s[0:1], s[78:79], 12
	s_ashr_i32 s2, s90, 31
	s_add_u32 s96, s0, s90
	s_addc_u32 s97, s1, s2
	v_mov_b32_e32 v151, v1
	s_mov_b64 s[0:1], 0
	s_cmpk_gt_i32 s90, 0xff
	s_mov_b64 s[30:31], -1
	s_cbranch_scc0 .LBB0_579
	s_lshr_b32 s0, s90, 8
	s_lshl_b64 s[20:21], s[96:97], 14
	s_add_u32 s20, s84, s20
	s_addc_u32 s21, s85, s21
	s_add_u32 s22, s20, 0x1000
	s_addc_u32 s23, s21, 0
	s_add_u32 s24, s20, 0x2000
	s_addc_u32 s25, s21, 0
	s_add_u32 s26, s20, 0x3000
	s_addc_u32 s27, s21, 0
	v_lshlrev_b32_e32 v116, 4, v151
	v_lshlrev_b32_e32 v109, 2, v151
	s_mov_b32 s44, 0x10001
	s_mov_b32 s45, 0x7060302
	v_mov_b32_e32 v108, 0x10001
	s_cmp_eq_u32 s98, 1
	s_cbranch_scc1 .Ltk_pref
	global_load_dwordx4 v[180:183], v116, s[20:21]
	global_load_dwordx4 v[184:187], v116, s[20:21] offset:1024
	s_cmp_lt_u32 s0, 2
	s_cbranch_scc1 .Ltk_z2
	global_load_dwordx4 v[188:191], v116, s[20:21] offset:2048
	s_cmp_lt_u32 s0, 3
	s_cbranch_scc1 .Ltk_z3
	global_load_dwordx4 v[192:195], v116, s[20:21] offset:3072
	s_cmp_lt_u32 s0, 4
	s_cbranch_scc1 .Ltk_z4
	global_load_dwordx4 v[196:199], v116, s[22:23]
	s_cmp_lt_u32 s0, 5
	s_cbranch_scc1 .Ltk_z5
	global_load_dwordx4 v[200:203], v116, s[22:23] offset:1024
	s_cmp_lt_u32 s0, 6
	s_cbranch_scc1 .Ltk_z6
	global_load_dwordx4 v[204:207], v116, s[22:23] offset:2048
	s_cmp_lt_u32 s0, 7
	s_cbranch_scc1 .Ltk_z7
	global_load_dwordx4 v[208:211], v116, s[22:23] offset:3072
	s_cmp_lt_u32 s0, 8
	s_cbranch_scc1 .Ltk_z8
	global_load_dwordx4 v[212:215], v116, s[24:25]
	s_cmp_lt_u32 s0, 9
	s_cbranch_scc1 .Ltk_z9
	global_load_dwordx4 v[216:219], v116, s[24:25] offset:1024
	s_cmp_lt_u32 s0, 10
	s_cbranch_scc1 .Ltk_z10
	global_load_dwordx4 v[220:223], v116, s[24:25] offset:2048
	s_cmp_lt_u32 s0, 11
	s_cbranch_scc1 .Ltk_z11
	global_load_dwordx4 v[224:227], v116, s[24:25] offset:3072
	s_cmp_lt_u32 s0, 12
	s_cbranch_scc1 .Ltk_z12
	global_load_dwordx4 v[228:231], v116, s[26:27]
	s_cmp_lt_u32 s0, 13
	s_cbranch_scc1 .Ltk_z13
	global_load_dwordx4 v[232:235], v116, s[26:27] offset:1024
	s_cmp_lt_u32 s0, 14
	s_cbranch_scc1 .Ltk_z14
	global_load_dwordx4 v[236:239], v116, s[26:27] offset:2048
	s_cmp_lt_u32 s0, 15
	s_cbranch_scc1 .Ltk_z15
	global_load_dwordx4 v[134:137], v116, s[26:27] offset:3072
	s_branch .Ltk_ld_done
.Ltk_pref:
	s_mov_b32 s98, 0
	s_cmp_lt_u32 s0, 2
	s_cbranch_scc1 .Ltk_z2
	s_cmp_lt_u32 s0, 3
	s_cbranch_scc1 .Ltk_z3
	s_cmp_lt_u32 s0, 4
	s_cbranch_scc1 .Ltk_z4
	s_cmp_lt_u32 s0, 5
	s_cbranch_scc1 .Ltk_z5
	s_cmp_lt_u32 s0, 6
	s_cbranch_scc1 .Ltk_z6
	s_cmp_lt_u32 s0, 7
	s_cbranch_scc1 .Ltk_z7
	s_cmp_lt_u32 s0, 8
	s_cbranch_scc1 .Ltk_z8
	s_cmp_lt_u32 s0, 9
	s_cbranch_scc1 .Ltk_z9
	s_cmp_lt_u32 s0, 10
	s_cbranch_scc1 .Ltk_z10
	s_cmp_lt_u32 s0, 11
	s_cbranch_scc1 .Ltk_z11
	s_cmp_lt_u32 s0, 12
	s_cbranch_scc1 .Ltk_z12
	s_cmp_lt_u32 s0, 13
	s_cbranch_scc1 .Ltk_z13
	s_cmp_lt_u32 s0, 14
	s_cbranch_scc1 .Ltk_z14
	s_cmp_lt_u32 s0, 15
	s_cbranch_scc1 .Ltk_z15
	s_branch .Ltk_ld_done
.Ltk_z2:
	v_mov_b32_e32 v188, 0
	v_mov_b32_e32 v189, 0
	v_mov_b32_e32 v190, 0
	v_mov_b32_e32 v191, 0
.Ltk_z3:
	v_mov_b32_e32 v192, 0
	v_mov_b32_e32 v193, 0
	v_mov_b32_e32 v194, 0
	v_mov_b32_e32 v195, 0
.Ltk_z4:
	v_mov_b32_e32 v196, 0
	v_mov_b32_e32 v197, 0
	v_mov_b32_e32 v198, 0
	v_mov_b32_e32 v199, 0
.Ltk_z5:
	v_mov_b32_e32 v200, 0
	v_mov_b32_e32 v201, 0
	v_mov_b32_e32 v202, 0
	v_mov_b32_e32 v203, 0
.Ltk_z6:
	v_mov_b32_e32 v204, 0
	v_mov_b32_e32 v205, 0
	v_mov_b32_e32 v206, 0
	v_mov_b32_e32 v207, 0
.Ltk_z7:
	v_mov_b32_e32 v208, 0
	v_mov_b32_e32 v209, 0
	v_mov_b32_e32 v210, 0
	v_mov_b32_e32 v211, 0
.Ltk_z8:
	v_mov_b32_e32 v212, 0
	v_mov_b32_e32 v213, 0
	v_mov_b32_e32 v214, 0
	v_mov_b32_e32 v215, 0
.Ltk_z9:
	v_mov_b32_e32 v216, 0
	v_mov_b32_e32 v217, 0
	v_mov_b32_e32 v218, 0
	v_mov_b32_e32 v219, 0
.Ltk_z10:
	v_mov_b32_e32 v220, 0
	v_mov_b32_e32 v221, 0
	v_mov_b32_e32 v222, 0
	v_mov_b32_e32 v223, 0
.Ltk_z11:
	v_mov_b32_e32 v224, 0
	v_mov_b32_e32 v225, 0
	v_mov_b32_e32 v226, 0
	v_mov_b32_e32 v227, 0
.Ltk_z12:
	v_mov_b32_e32 v228, 0
	v_mov_b32_e32 v229, 0
	v_mov_b32_e32 v230, 0
	v_mov_b32_e32 v231, 0
.Ltk_z13:
	v_mov_b32_e32 v232, 0
	v_mov_b32_e32 v233, 0
	v_mov_b32_e32 v234, 0
	v_mov_b32_e32 v235, 0
.Ltk_z14:
	v_mov_b32_e32 v236, 0
	v_mov_b32_e32 v237, 0
	v_mov_b32_e32 v238, 0
	v_mov_b32_e32 v239, 0
.Ltk_z15:
	v_mov_b32_e32 v134, 0
	v_mov_b32_e32 v135, 0
	v_mov_b32_e32 v136, 0
	v_mov_b32_e32 v137, 0
.Ltk_ld_done:
	s_lshl_b32 s15, s0, 8
	s_sub_u32 s15, s90, s15
	v_sub_u32_e32 v115, s15, v109
	s_waitcnt vmcnt(0)
	v_ashrrev_i32_e32 v98, 31, v180
	v_ashrrev_i32_e32 v99, 31, v181
	v_ashrrev_i32_e32 v100, 31, v182
	v_ashrrev_i32_e32 v101, 31, v183
	v_or_b32_e32 v98, 0x80000000, v98
	v_or_b32_e32 v99, 0x80000000, v99
	v_or_b32_e32 v100, 0x80000000, v100
	v_or_b32_e32 v101, 0x80000000, v101
	v_xor_b32_e32 v180, v98, v180
	v_xor_b32_e32 v181, v99, v181
	v_xor_b32_e32 v182, v100, v182
	v_xor_b32_e32 v183, v101, v183
	v_ashrrev_i32_e32 v98, 31, v184
	v_ashrrev_i32_e32 v99, 31, v185
	v_ashrrev_i32_e32 v100, 31, v186
	v_ashrrev_i32_e32 v101, 31, v187
	v_or_b32_e32 v98, 0x80000000, v98
	v_or_b32_e32 v99, 0x80000000, v99
	v_or_b32_e32 v100, 0x80000000, v100
	v_or_b32_e32 v101, 0x80000000, v101
	v_xor_b32_e32 v184, v98, v184
	v_xor_b32_e32 v185, v99, v185
	v_xor_b32_e32 v186, v100, v186
	v_xor_b32_e32 v187, v101, v187
	s_cmp_lt_u32 s0, 2
	s_cbranch_scc1 .Ltk_tr_done
	v_ashrrev_i32_e32 v98, 31, v188
	v_ashrrev_i32_e32 v99, 31, v189
	v_ashrrev_i32_e32 v100, 31, v190
	v_ashrrev_i32_e32 v101, 31, v191
	v_or_b32_e32 v98, 0x80000000, v98
	v_or_b32_e32 v99, 0x80000000, v99
	v_or_b32_e32 v100, 0x80000000, v100
	v_or_b32_e32 v101, 0x80000000, v101
	v_xor_b32_e32 v188, v98, v188
	v_xor_b32_e32 v189, v99, v189
	v_xor_b32_e32 v190, v100, v190
	v_xor_b32_e32 v191, v101, v191
	s_cmp_lt_u32 s0, 3
	s_cbranch_scc1 .Ltk_tr_done
	v_ashrrev_i32_e32 v98, 31, v192
	v_ashrrev_i32_e32 v99, 31, v193
	v_ashrrev_i32_e32 v100, 31, v194
	v_ashrrev_i32_e32 v101, 31, v195
	v_or_b32_e32 v98, 0x80000000, v98
	v_or_b32_e32 v99, 0x80000000, v99
	v_or_b32_e32 v100, 0x80000000, v100
	v_or_b32_e32 v101, 0x80000000, v101
	v_xor_b32_e32 v192, v98, v192
	v_xor_b32_e32 v193, v99, v193
	v_xor_b32_e32 v194, v100, v194
	v_xor_b32_e32 v195, v101, v195
	s_cmp_lt_u32 s0, 4
	s_cbranch_scc1 .Ltk_tr_done
	v_ashrrev_i32_e32 v98, 31, v196
	v_ashrrev_i32_e32 v99, 31, v197
	v_ashrrev_i32_e32 v100, 31, v198
	v_ashrrev_i32_e32 v101, 31, v199
	v_or_b32_e32 v98, 0x80000000, v98
	v_or_b32_e32 v99, 0x80000000, v99
	v_or_b32_e32 v100, 0x80000000, v100
	v_or_b32_e32 v101, 0x80000000, v101
	v_xor_b32_e32 v196, v98, v196
	v_xor_b32_e32 v197, v99, v197
	v_xor_b32_e32 v198, v100, v198
	v_xor_b32_e32 v199, v101, v199
	s_cmp_lt_u32 s0, 5
	s_cbranch_scc1 .Ltk_tr_done
	v_ashrrev_i32_e32 v98, 31, v200
	v_ashrrev_i32_e32 v99, 31, v201
	v_ashrrev_i32_e32 v100, 31, v202
	v_ashrrev_i32_e32 v101, 31, v203
	v_or_b32_e32 v98, 0x80000000, v98
	v_or_b32_e32 v99, 0x80000000, v99
	v_or_b32_e32 v100, 0x80000000, v100
	v_or_b32_e32 v101, 0x80000000, v101
	v_xor_b32_e32 v200, v98, v200
	v_xor_b32_e32 v201, v99, v201
	v_xor_b32_e32 v202, v100, v202
	v_xor_b32_e32 v203, v101, v203
	s_cmp_lt_u32 s0, 6
	s_cbranch_scc1 .Ltk_tr_done
	v_ashrrev_i32_e32 v98, 31, v204
	v_ashrrev_i32_e32 v99, 31, v205
	v_ashrrev_i32_e32 v100, 31, v206
	v_ashrrev_i32_e32 v101, 31, v207
	v_or_b32_e32 v98, 0x80000000, v98
	v_or_b32_e32 v99, 0x80000000, v99
	v_or_b32_e32 v100, 0x80000000, v100
	v_or_b32_e32 v101, 0x80000000, v101
	v_xor_b32_e32 v204, v98, v204
	v_xor_b32_e32 v205, v99, v205
	v_xor_b32_e32 v206, v100, v206
	v_xor_b32_e32 v207, v101, v207
	s_cmp_lt_u32 s0, 7
	s_cbranch_scc1 .Ltk_tr_done
	v_ashrrev_i32_e32 v98, 31, v208
	v_ashrrev_i32_e32 v99, 31, v209
	v_ashrrev_i32_e32 v100, 31, v210
	v_ashrrev_i32_e32 v101, 31, v211
	v_or_b32_e32 v98, 0x80000000, v98
	v_or_b32_e32 v99, 0x80000000, v99
	v_or_b32_e32 v100, 0x80000000, v100
	v_or_b32_e32 v101, 0x80000000, v101
	v_xor_b32_e32 v208, v98, v208
	v_xor_b32_e32 v209, v99, v209
	v_xor_b32_e32 v210, v100, v210
	v_xor_b32_e32 v211, v101, v211
	s_cmp_lt_u32 s0, 8
	s_cbranch_scc1 .Ltk_tr_done
	v_ashrrev_i32_e32 v98, 31, v212
	v_ashrrev_i32_e32 v99, 31, v213
	v_ashrrev_i32_e32 v100, 31, v214
	v_ashrrev_i32_e32 v101, 31, v215
	v_or_b32_e32 v98, 0x80000000, v98
	v_or_b32_e32 v99, 0x80000000, v99
	v_or_b32_e32 v100, 0x80000000, v100
	v_or_b32_e32 v101, 0x80000000, v101
	v_xor_b32_e32 v212, v98, v212
	v_xor_b32_e32 v213, v99, v213
	v_xor_b32_e32 v214, v100, v214
	v_xor_b32_e32 v215, v101, v215
	s_cmp_lt_u32 s0, 9
	s_cbranch_scc1 .Ltk_tr_done
	v_ashrrev_i32_e32 v98, 31, v216
	v_ashrrev_i32_e32 v99, 31, v217
	v_ashrrev_i32_e32 v100, 31, v218
	v_ashrrev_i32_e32 v101, 31, v219
	v_or_b32_e32 v98, 0x80000000, v98
	v_or_b32_e32 v99, 0x80000000, v99
	v_or_b32_e32 v100, 0x80000000, v100
	v_or_b32_e32 v101, 0x80000000, v101
	v_xor_b32_e32 v216, v98, v216
	v_xor_b32_e32 v217, v99, v217
	v_xor_b32_e32 v218, v100, v218
	v_xor_b32_e32 v219, v101, v219
	s_cmp_lt_u32 s0, 10
	s_cbranch_scc1 .Ltk_tr_done
	v_ashrrev_i32_e32 v98, 31, v220
	v_ashrrev_i32_e32 v99, 31, v221
	v_ashrrev_i32_e32 v100, 31, v222
	v_ashrrev_i32_e32 v101, 31, v223
	v_or_b32_e32 v98, 0x80000000, v98
	v_or_b32_e32 v99, 0x80000000, v99
	v_or_b32_e32 v100, 0x80000000, v100
	v_or_b32_e32 v101, 0x80000000, v101
	v_xor_b32_e32 v220, v98, v220
	v_xor_b32_e32 v221, v99, v221
	v_xor_b32_e32 v222, v100, v222
	v_xor_b32_e32 v223, v101, v223
	s_cmp_lt_u32 s0, 11
	s_cbranch_scc1 .Ltk_tr_done
	v_ashrrev_i32_e32 v98, 31, v224
	v_ashrrev_i32_e32 v99, 31, v225
	v_ashrrev_i32_e32 v100, 31, v226
	v_ashrrev_i32_e32 v101, 31, v227
	v_or_b32_e32 v98, 0x80000000, v98
	v_or_b32_e32 v99, 0x80000000, v99
	v_or_b32_e32 v100, 0x80000000, v100
	v_or_b32_e32 v101, 0x80000000, v101
	v_xor_b32_e32 v224, v98, v224
	v_xor_b32_e32 v225, v99, v225
	v_xor_b32_e32 v226, v100, v226
	v_xor_b32_e32 v227, v101, v227
	s_cmp_lt_u32 s0, 12
	s_cbranch_scc1 .Ltk_tr_done
	v_ashrrev_i32_e32 v98, 31, v228
	v_ashrrev_i32_e32 v99, 31, v229
	v_ashrrev_i32_e32 v100, 31, v230
	v_ashrrev_i32_e32 v101, 31, v231
	v_or_b32_e32 v98, 0x80000000, v98
	v_or_b32_e32 v99, 0x80000000, v99
	v_or_b32_e32 v100, 0x80000000, v100
	v_or_b32_e32 v101, 0x80000000, v101
	v_xor_b32_e32 v228, v98, v228
	v_xor_b32_e32 v229, v99, v229
	v_xor_b32_e32 v230, v100, v230
	v_xor_b32_e32 v231, v101, v231
	s_cmp_lt_u32 s0, 13
	s_cbranch_scc1 .Ltk_tr_done
	v_ashrrev_i32_e32 v98, 31, v232
	v_ashrrev_i32_e32 v99, 31, v233
	v_ashrrev_i32_e32 v100, 31, v234
	v_ashrrev_i32_e32 v101, 31, v235
	v_or_b32_e32 v98, 0x80000000, v98
	v_or_b32_e32 v99, 0x80000000, v99
	v_or_b32_e32 v100, 0x80000000, v100
	v_or_b32_e32 v101, 0x80000000, v101
	v_xor_b32_e32 v232, v98, v232
	v_xor_b32_e32 v233, v99, v233
	v_xor_b32_e32 v234, v100, v234
	v_xor_b32_e32 v235, v101, v235
	s_cmp_lt_u32 s0, 14
	s_cbranch_scc1 .Ltk_tr_done
	v_ashrrev_i32_e32 v98, 31, v236
	v_ashrrev_i32_e32 v99, 31, v237
	v_ashrrev_i32_e32 v100, 31, v238
	v_ashrrev_i32_e32 v101, 31, v239
	v_or_b32_e32 v98, 0x80000000, v98
	v_or_b32_e32 v99, 0x80000000, v99
	v_or_b32_e32 v100, 0x80000000, v100
	v_or_b32_e32 v101, 0x80000000, v101
	v_xor_b32_e32 v236, v98, v236
	v_xor_b32_e32 v237, v99, v237
	v_xor_b32_e32 v238, v100, v238
	v_xor_b32_e32 v239, v101, v239
	s_cmp_lt_u32 s0, 15
	s_cbranch_scc1 .Ltk_tr_done
	v_ashrrev_i32_e32 v98, 31, v134
	v_ashrrev_i32_e32 v99, 31, v135
	v_ashrrev_i32_e32 v100, 31, v136
	v_ashrrev_i32_e32 v101, 31, v137
	v_or_b32_e32 v98, 0x80000000, v98
	v_or_b32_e32 v99, 0x80000000, v99
	v_or_b32_e32 v100, 0x80000000, v100
	v_or_b32_e32 v101, 0x80000000, v101
	v_xor_b32_e32 v134, v98, v134
	v_xor_b32_e32 v135, v99, v135
	v_xor_b32_e32 v136, v100, v136
	v_xor_b32_e32 v137, v101, v137

.Ltk_mk1:
	v_cmp_le_i32_e64 s[20:21], 0, v115
	v_cmp_le_i32_e64 s[22:23], 1, v115
	v_cmp_le_i32_e64 s[24:25], 2, v115
	v_cmp_le_i32_e64 s[26:27], 3, v115
	v_cndmask_b32_e64 v184, 0, v184, s[20:21]
	v_cndmask_b32_e64 v185, 0, v185, s[22:23]
	v_cndmask_b32_e64 v186, 0, v186, s[24:25]
	v_cndmask_b32_e64 v187, 0, v187, s[26:27]
	s_branch .Ltk_mk_done
.Ltk_mk2:
	v_cmp_le_i32_e64 s[20:21], 0, v115
	v_cmp_le_i32_e64 s[22:23], 1, v115
	v_cmp_le_i32_e64 s[24:25], 2, v115
	v_cmp_le_i32_e64 s[26:27], 3, v115
	v_cndmask_b32_e64 v188, 0, v188, s[20:21]
	v_cndmask_b32_e64 v189, 0, v189, s[22:23]
	v_cndmask_b32_e64 v190, 0, v190, s[24:25]
	v_cndmask_b32_e64 v191, 0, v191, s[26:27]
	s_branch .Ltk_mk_done
.Ltk_mk3:
	v_cmp_le_i32_e64 s[20:21], 0, v115
	v_cmp_le_i32_e64 s[22:23], 1, v115
	v_cmp_le_i32_e64 s[24:25], 2, v115
	v_cmp_le_i32_e64 s[26:27], 3, v115
	v_cndmask_b32_e64 v192, 0, v192, s[20:21]
	v_cndmask_b32_e64 v193, 0, v193, s[22:23]
	v_cndmask_b32_e64 v194, 0, v194, s[24:25]
	v_cndmask_b32_e64 v195, 0, v195, s[26:27]
	s_branch .Ltk_mk_done
.Ltk_mk4:
	v_cmp_le_i32_e64 s[20:21], 0, v115
	v_cmp_le_i32_e64 s[22:23], 1, v115
	v_cmp_le_i32_e64 s[24:25], 2, v115
	v_cmp_le_i32_e64 s[26:27], 3, v115
	v_cndmask_b32_e64 v196, 0, v196, s[20:21]
	v_cndmask_b32_e64 v197, 0, v197, s[22:23]
	v_cndmask_b32_e64 v198, 0, v198, s[24:25]
	v_cndmask_b32_e64 v199, 0, v199, s[26:27]
	s_branch .Ltk_mk_done
.Ltk_mk5:
	v_cmp_le_i32_e64 s[20:21], 0, v115
	v_cmp_le_i32_e64 s[22:23], 1, v115
	v_cmp_le_i32_e64 s[24:25], 2, v115
	v_cmp_le_i32_e64 s[26:27], 3, v115
	v_cndmask_b32_e64 v200, 0, v200, s[20:21]
	v_cndmask_b32_e64 v201, 0, v201, s[22:23]
	v_cndmask_b32_e64 v202, 0, v202, s[24:25]
	v_cndmask_b32_e64 v203, 0, v203, s[26:27]
	s_branch .Ltk_mk_done
.Ltk_mk6:
	v_cmp_le_i32_e64 s[20:21], 0, v115
	v_cmp_le_i32_e64 s[22:23], 1, v115
	v_cmp_le_i32_e64 s[24:25], 2, v115
	v_cmp_le_i32_e64 s[26:27], 3, v115
	v_cndmask_b32_e64 v204, 0, v204, s[20:21]
	v_cndmask_b32_e64 v205, 0, v205, s[22:23]
	v_cndmask_b32_e64 v206, 0, v206, s[24:25]
	v_cndmask_b32_e64 v207, 0, v207, s[26:27]
	s_branch .Ltk_mk_done
.Ltk_mk7:
	v_cmp_le_i32_e64 s[20:21], 0, v115
	v_cmp_le_i32_e64 s[22:23], 1, v115
	v_cmp_le_i32_e64 s[24:25], 2, v115
	v_cmp_le_i32_e64 s[26:27], 3, v115
	v_cndmask_b32_e64 v208, 0, v208, s[20:21]
	v_cndmask_b32_e64 v209, 0, v209, s[22:23]
	v_cndmask_b32_e64 v210, 0, v210, s[24:25]
	v_cndmask_b32_e64 v211, 0, v211, s[26:27]
	s_branch .Ltk_mk_done
.Ltk_mk8:
	v_cmp_le_i32_e64 s[20:21], 0, v115
	v_cmp_le_i32_e64 s[22:23], 1, v115
	v_cmp_le_i32_e64 s[24:25], 2, v115
	v_cmp_le_i32_e64 s[26:27], 3, v115
	v_cndmask_b32_e64 v212, 0, v212, s[20:21]
	v_cndmask_b32_e64 v213, 0, v213, s[22:23]
	v_cndmask_b32_e64 v214, 0, v214, s[24:25]
	v_cndmask_b32_e64 v215, 0, v215, s[26:27]
	s_branch .Ltk_mk_done
.Ltk_mk9:
	v_cmp_le_i32_e64 s[20:21], 0, v115
	v_cmp_le_i32_e64 s[22:23], 1, v115
	v_cmp_le_i32_e64 s[24:25], 2, v115
	v_cmp_le_i32_e64 s[26:27], 3, v115
	v_cndmask_b32_e64 v216, 0, v216, s[20:21]
	v_cndmask_b32_e64 v217, 0, v217, s[22:23]
	v_cndmask_b32_e64 v218, 0, v218, s[24:25]
	v_cndmask_b32_e64 v219, 0, v219, s[26:27]
	s_branch .Ltk_mk_done
.Ltk_mk10:
	v_cmp_le_i32_e64 s[20:21], 0, v115
	v_cmp_le_i32_e64 s[22:23], 1, v115
	v_cmp_le_i32_e64 s[24:25], 2, v115
	v_cmp_le_i32_e64 s[26:27], 3, v115
	v_cndmask_b32_e64 v220, 0, v220, s[20:21]
	v_cndmask_b32_e64 v221, 0, v221, s[22:23]
	v_cndmask_b32_e64 v222, 0, v222, s[24:25]
	v_cndmask_b32_e64 v223, 0, v223, s[26:27]
	s_branch .Ltk_mk_done
.Ltk_mk11:
	v_cmp_le_i32_e64 s[20:21], 0, v115
	v_cmp_le_i32_e64 s[22:23], 1, v115
	v_cmp_le_i32_e64 s[24:25], 2, v115
	v_cmp_le_i32_e64 s[26:27], 3, v115
	v_cndmask_b32_e64 v224, 0, v224, s[20:21]
	v_cndmask_b32_e64 v225, 0, v225, s[22:23]
	v_cndmask_b32_e64 v226, 0, v226, s[24:25]
	v_cndmask_b32_e64 v227, 0, v227, s[26:27]
	s_branch .Ltk_mk_done
.Ltk_mk12:
	v_cmp_le_i32_e64 s[20:21], 0, v115
	v_cmp_le_i32_e64 s[22:23], 1, v115
	v_cmp_le_i32_e64 s[24:25], 2, v115
	v_cmp_le_i32_e64 s[26:27], 3, v115
	v_cndmask_b32_e64 v228, 0, v228, s[20:21]
	v_cndmask_b32_e64 v229, 0, v229, s[22:23]
	v_cndmask_b32_e64 v230, 0, v230, s[24:25]
	v_cndmask_b32_e64 v231, 0, v231, s[26:27]
	s_branch .Ltk_mk_done
.Ltk_mk13:
	v_cmp_le_i32_e64 s[20:21], 0, v115
	v_cmp_le_i32_e64 s[22:23], 1, v115
	v_cmp_le_i32_e64 s[24:25], 2, v115
	v_cmp_le_i32_e64 s[26:27], 3, v115
	v_cndmask_b32_e64 v232, 0, v232, s[20:21]
	v_cndmask_b32_e64 v233, 0, v233, s[22:23]
	v_cndmask_b32_e64 v234, 0, v234, s[24:25]
	v_cndmask_b32_e64 v235, 0, v235, s[26:27]
	s_branch .Ltk_mk_done
.Ltk_mk14:
	v_cmp_le_i32_e64 s[20:21], 0, v115
	v_cmp_le_i32_e64 s[22:23], 1, v115
	v_cmp_le_i32_e64 s[24:25], 2, v115
	v_cmp_le_i32_e64 s[26:27], 3, v115
	v_cndmask_b32_e64 v236, 0, v236, s[20:21]
	v_cndmask_b32_e64 v237, 0, v237, s[22:23]
	v_cndmask_b32_e64 v238, 0, v238, s[24:25]
	v_cndmask_b32_e64 v239, 0, v239, s[26:27]
	s_branch .Ltk_mk_done
.Ltk_mk15:
	v_cmp_le_i32_e64 s[20:21], 0, v115
	v_cmp_le_i32_e64 s[22:23], 1, v115
	v_cmp_le_i32_e64 s[24:25], 2, v115
	v_cmp_le_i32_e64 s[26:27], 3, v115
	v_cndmask_b32_e64 v134, 0, v134, s[20:21]
	v_cndmask_b32_e64 v135, 0, v135, s[22:23]
	v_cndmask_b32_e64 v136, 0, v136, s[24:25]
	v_cndmask_b32_e64 v137, 0, v137, s[26:27]
.Ltk_mk_done:
	v_perm_b32 v66, v181, v180, s45
	v_perm_b32 v67, v183, v182, s45
	v_perm_b32 v68, v185, v184, s45
	v_perm_b32 v69, v187, v186, s45
	v_perm_b32 v70, v189, v188, s45
	v_perm_b32 v71, v191, v190, s45
	v_perm_b32 v72, v193, v192, s45
	v_perm_b32 v73, v195, v194, s45
	v_perm_b32 v74, v197, v196, s45
	v_perm_b32 v75, v199, v198, s45
	v_perm_b32 v76, v201, v200, s45
	v_perm_b32 v77, v203, v202, s45
	v_perm_b32 v78, v205, v204, s45
	v_perm_b32 v79, v207, v206, s45
	v_perm_b32 v80, v209, v208, s45
	v_perm_b32 v81, v211, v210, s45
	v_perm_b32 v82, v213, v212, s45
	v_perm_b32 v83, v215, v214, s45
	v_perm_b32 v84, v217, v216, s45
	v_perm_b32 v85, v219, v218, s45
	v_perm_b32 v86, v221, v220, s45
	v_perm_b32 v87, v223, v222, s45
	v_perm_b32 v88, v225, v224, s45
	v_perm_b32 v89, v227, v226, s45
	v_perm_b32 v90, v229, v228, s45
	v_perm_b32 v91, v231, v230, s45
	v_perm_b32 v92, v233, v232, s45
	v_perm_b32 v93, v235, v234, s45
	v_perm_b32 v94, v237, v236, s45
	v_perm_b32 v95, v239, v238, s45
	v_perm_b32 v96, v135, v134, s45
	v_perm_b32 v97, v137, v136, s45
	s_lshr_b32 s31, s0, 2
	s_mov_b32 s1, 0
	s_mov_b32 s4, 0x8000
	s_mov_b32 s30, 0
	s_mov_b32 s10, 0

.Ltk_ngt_dec:
	s_sub_u32 s8, 0x100, s7
	s_mul_i32 s15, s1, s44
	s_mov_b32 s45, 0x5040100
	v_xor_b32_e32 v98, s15, v66
	v_pk_min_u16 v98, v98, v108
	v_pk_sub_u16 v98, v98, v108
	v_perm_b32 v66, v181, v180, s45
	v_and_b32_e32 v66, v98, v66
	v_xor_b32_e32 v99, s15, v67
	v_pk_min_u16 v99, v99, v108
	v_pk_sub_u16 v99, v99, v108
	v_perm_b32 v67, v183, v182, s45
	v_and_b32_e32 v67, v99, v67
	v_xor_b32_e32 v100, s15, v68
	v_pk_min_u16 v100, v100, v108
	v_pk_sub_u16 v100, v100, v108
	v_perm_b32 v68, v185, v184, s45
	v_and_b32_e32 v68, v100, v68
	v_xor_b32_e32 v101, s15, v69
	v_pk_min_u16 v101, v101, v108
	v_pk_sub_u16 v101, v101, v108
	v_perm_b32 v69, v187, v186, s45
	v_and_b32_e32 v69, v101, v69
	v_xor_b32_e32 v98, s15, v70
	v_pk_min_u16 v98, v98, v108
	v_pk_sub_u16 v98, v98, v108
	v_perm_b32 v70, v189, v188, s45
	v_and_b32_e32 v70, v98, v70
	v_xor_b32_e32 v99, s15, v71
	v_pk_min_u16 v99, v99, v108
	v_pk_sub_u16 v99, v99, v108
	v_perm_b32 v71, v191, v190, s45
	v_and_b32_e32 v71, v99, v71
	v_xor_b32_e32 v100, s15, v72
	v_pk_min_u16 v100, v100, v108
	v_pk_sub_u16 v100, v100, v108
	v_perm_b32 v72, v193, v192, s45
	v_and_b32_e32 v72, v100, v72
	v_xor_b32_e32 v101, s15, v73
	v_pk_min_u16 v101, v101, v108
	v_pk_sub_u16 v101, v101, v108
	v_perm_b32 v73, v195, v194, s45
	v_and_b32_e32 v73, v101, v73
	s_cmp_eq_u32 s31, 0
	s_cbranch_scc1 .Ltk_lo_start
	v_xor_b32_e32 v98, s15, v74
	v_pk_min_u16 v98, v98, v108
	v_pk_sub_u16 v98, v98, v108
	v_perm_b32 v74, v197, v196, s45
	v_and_b32_e32 v74, v98, v74
	v_xor_b32_e32 v99, s15, v75
	v_pk_min_u16 v99, v99, v108
	v_pk_sub_u16 v99, v99, v108
	v_perm_b32 v75, v199, v198, s45
	v_and_b32_e32 v75, v99, v75
	v_xor_b32_e32 v100, s15, v76
	v_pk_min_u16 v100, v100, v108
	v_pk_sub_u16 v100, v100, v108
	v_perm_b32 v76, v201, v200, s45
	v_and_b32_e32 v76, v100, v76
	v_xor_b32_e32 v101, s15, v77
	v_pk_min_u16 v101, v101, v108
	v_pk_sub_u16 v101, v101, v108
	v_perm_b32 v77, v203, v202, s45
	v_and_b32_e32 v77, v101, v77
	v_xor_b32_e32 v98, s15, v78
	v_pk_min_u16 v98, v98, v108
	v_pk_sub_u16 v98, v98, v108
	v_perm_b32 v78, v205, v204, s45
	v_and_b32_e32 v78, v98, v78
	v_xor_b32_e32 v99, s15, v79
	v_pk_min_u16 v99, v99, v108
	v_pk_sub_u16 v99, v99, v108
	v_perm_b32 v79, v207, v206, s45
	v_and_b32_e32 v79, v99, v79
	v_xor_b32_e32 v100, s15, v80
	v_pk_min_u16 v100, v100, v108
	v_pk_sub_u16 v100, v100, v108
	v_perm_b32 v80, v209, v208, s45
	v_and_b32_e32 v80, v100, v80
	v_xor_b32_e32 v101, s15, v81
	v_pk_min_u16 v101, v101, v108
	v_pk_sub_u16 v101, v101, v108
	v_perm_b32 v81, v211, v210, s45
	v_and_b32_e32 v81, v101, v81
	s_cmp_eq_u32 s31, 1
	s_cbranch_scc1 .Ltk_lo_start
	v_xor_b32_e32 v98, s15, v82
	v_pk_min_u16 v98, v98, v108
	v_pk_sub_u16 v98, v98, v108
	v_perm_b32 v82, v213, v212, s45
	v_and_b32_e32 v82, v98, v82
	v_xor_b32_e32 v99, s15, v83
	v_pk_min_u16 v99, v99, v108
	v_pk_sub_u16 v99, v99, v108
	v_perm_b32 v83, v215, v214, s45
	v_and_b32_e32 v83, v99, v83
	v_xor_b32_e32 v100, s15, v84
	v_pk_min_u16 v100, v100, v108
	v_pk_sub_u16 v100, v100, v108
	v_perm_b32 v84, v217, v216, s45
	v_and_b32_e32 v84, v100, v84
	v_xor_b32_e32 v101, s15, v85
	v_pk_min_u16 v101, v101, v108
	v_pk_sub_u16 v101, v101, v108
	v_perm_b32 v85, v219, v218, s45
	v_and_b32_e32 v85, v101, v85
	v_xor_b32_e32 v98, s15, v86
	v_pk_min_u16 v98, v98, v108
	v_pk_sub_u16 v98, v98, v108
	v_perm_b32 v86, v221, v220, s45
	v_and_b32_e32 v86, v98, v86
	v_xor_b32_e32 v99, s15, v87
	v_pk_min_u16 v99, v99, v108
	v_pk_sub_u16 v99, v99, v108
	v_perm_b32 v87, v223, v222, s45
	v_and_b32_e32 v87, v99, v87
	v_xor_b32_e32 v100, s15, v88
	v_pk_min_u16 v100, v100, v108
	v_pk_sub_u16 v100, v100, v108
	v_perm_b32 v88, v225, v224, s45
	v_and_b32_e32 v88, v100, v88
	v_xor_b32_e32 v101, s15, v89
	v_pk_min_u16 v101, v101, v108
	v_pk_sub_u16 v101, v101, v108
	v_perm_b32 v89, v227, v226, s45
	v_and_b32_e32 v89, v101, v89
	s_cmp_eq_u32 s31, 2
	s_cbranch_scc1 .Ltk_lo_start
	v_xor_b32_e32 v98, s15, v90
	v_pk_min_u16 v98, v98, v108
	v_pk_sub_u16 v98, v98, v108
	v_perm_b32 v90, v229, v228, s45
	v_and_b32_e32 v90, v98, v90
	v_xor_b32_e32 v99, s15, v91
	v_pk_min_u16 v99, v99, v108
	v_pk_sub_u16 v99, v99, v108
	v_perm_b32 v91, v231, v230, s45
	v_and_b32_e32 v91, v99, v91
	v_xor_b32_e32 v100, s15, v92
	v_pk_min_u16 v100, v100, v108
	v_pk_sub_u16 v100, v100, v108
	v_perm_b32 v92, v233, v232, s45
	v_and_b32_e32 v92, v100, v92
	v_xor_b32_e32 v101, s15, v93
	v_pk_min_u16 v101, v101, v108
	v_pk_sub_u16 v101, v101, v108
	v_perm_b32 v93, v235, v234, s45
	v_and_b32_e32 v93, v101, v93
	v_xor_b32_e32 v98, s15, v94
	v_pk_min_u16 v98, v98, v108
	v_pk_sub_u16 v98, v98, v108
	v_perm_b32 v94, v237, v236, s45
	v_and_b32_e32 v94, v98, v94
	v_xor_b32_e32 v99, s15, v95
	v_pk_min_u16 v99, v99, v108
	v_pk_sub_u16 v99, v99, v108
	v_perm_b32 v95, v239, v238, s45
	v_and_b32_e32 v95, v99, v95
	v_xor_b32_e32 v100, s15, v96
	v_pk_min_u16 v100, v100, v108
	v_pk_sub_u16 v100, v100, v108
	v_perm_b32 v96, v135, v134, s45
	v_and_b32_e32 v96, v100, v96
	v_xor_b32_e32 v101, s15, v97
	v_pk_min_u16 v101, v101, v108
	v_pk_sub_u16 v101, v101, v108
	v_perm_b32 v97, v137, v136, s45
	v_and_b32_e32 v97, v101, v97

.Ltk_select:
	v_mov_b32_e32 v110, s15
	v_mov_b32_e32 v114, 0
	s_movk_i32 s29, 0x100
	v_cmp_ge_u32_e64 s[20:21], v180, v110
	v_cmp_ge_u32_e64 s[22:23], v181, v110
	v_cmp_ge_u32_e64 s[24:25], v182, v110
	v_cmp_ge_u32_e64 s[26:27], v183, v110
	s_bcnt1_i32_b64 s28, s[20:21]
	v_mbcnt_lo_u32_b32 v111, s20, v114
	v_mbcnt_hi_u32_b32 v111, s21, v111
	v_add_u32_e32 v113, 0, v109
	v_lshl_add_u32 v112, v111, 2, s89
	s_mov_b64 exec, s[20:21]
	ds_write_b32 v112, v113
	s_mov_b64 exec, -1
	v_add_u32_e32 v114, s28, v114
	s_bcnt1_i32_b64 s28, s[22:23]
	v_mbcnt_lo_u32_b32 v111, s22, v114
	v_mbcnt_hi_u32_b32 v111, s23, v111
	v_add_u32_e32 v113, 1, v109
	v_lshl_add_u32 v112, v111, 2, s89
	s_mov_b64 exec, s[22:23]
	ds_write_b32 v112, v113
	s_mov_b64 exec, -1
	v_add_u32_e32 v114, s28, v114
	s_bcnt1_i32_b64 s28, s[24:25]
	v_mbcnt_lo_u32_b32 v111, s24, v114
	v_mbcnt_hi_u32_b32 v111, s25, v111
	v_add_u32_e32 v113, 2, v109
	v_lshl_add_u32 v112, v111, 2, s89
	s_mov_b64 exec, s[24:25]
	ds_write_b32 v112, v113
	s_mov_b64 exec, -1
	v_add_u32_e32 v114, s28, v114
	s_bcnt1_i32_b64 s28, s[26:27]
	v_mbcnt_lo_u32_b32 v111, s26, v114
	v_mbcnt_hi_u32_b32 v111, s27, v111
	v_add_u32_e32 v113, 3, v109
	v_lshl_add_u32 v112, v111, 2, s89
	s_mov_b64 exec, s[26:27]
	ds_write_b32 v112, v113
	s_mov_b64 exec, -1
	v_add_u32_e32 v114, s28, v114
	v_cmp_ge_u32_e64 s[20:21], v184, v110
	v_cmp_ge_u32_e64 s[22:23], v185, v110
	v_cmp_ge_u32_e64 s[24:25], v186, v110
	v_cmp_ge_u32_e64 s[26:27], v187, v110
	s_bcnt1_i32_b64 s28, s[20:21]
	v_mbcnt_lo_u32_b32 v111, s20, v114
	v_mbcnt_hi_u32_b32 v111, s21, v111
	v_add_u32_e32 v113, 0x100, v109
	v_lshl_add_u32 v112, v111, 2, s89
	s_mov_b64 exec, s[20:21]
	ds_write_b32 v112, v113
	s_mov_b64 exec, -1
	v_add_u32_e32 v114, s28, v114
	s_bcnt1_i32_b64 s28, s[22:23]
	v_mbcnt_lo_u32_b32 v111, s22, v114
	v_mbcnt_hi_u32_b32 v111, s23, v111
	v_add_u32_e32 v113, 0x101, v109
	v_lshl_add_u32 v112, v111, 2, s89
	s_mov_b64 exec, s[22:23]
	ds_write_b32 v112, v113
	s_mov_b64 exec, -1
	v_add_u32_e32 v114, s28, v114
	s_bcnt1_i32_b64 s28, s[24:25]
	v_mbcnt_lo_u32_b32 v111, s24, v114
	v_mbcnt_hi_u32_b32 v111, s25, v111
	v_add_u32_e32 v113, 0x102, v109
	v_lshl_add_u32 v112, v111, 2, s89
	s_mov_b64 exec, s[24:25]
	ds_write_b32 v112, v113
	s_mov_b64 exec, -1
	v_add_u32_e32 v114, s28, v114
	s_bcnt1_i32_b64 s28, s[26:27]
	v_mbcnt_lo_u32_b32 v111, s26, v114
	v_mbcnt_hi_u32_b32 v111, s27, v111
	v_add_u32_e32 v113, 0x103, v109
	v_lshl_add_u32 v112, v111, 2, s89
	s_mov_b64 exec, s[26:27]
	ds_write_b32 v112, v113
	s_mov_b64 exec, -1
	v_add_u32_e32 v114, s28, v114
	s_cmp_lt_u32 s0, 2
	s_cbranch_scc1 .Ltk_p1_done
	v_cmp_ge_u32_e64 s[20:21], v188, v110
	v_cmp_ge_u32_e64 s[22:23], v189, v110
	v_cmp_ge_u32_e64 s[24:25], v190, v110
	v_cmp_ge_u32_e64 s[26:27], v191, v110
	s_bcnt1_i32_b64 s28, s[20:21]
	v_mbcnt_lo_u32_b32 v111, s20, v114
	v_mbcnt_hi_u32_b32 v111, s21, v111
	v_add_u32_e32 v113, 0x200, v109
	v_lshl_add_u32 v112, v111, 2, s89
	s_mov_b64 exec, s[20:21]
	ds_write_b32 v112, v113
	s_mov_b64 exec, -1
	v_add_u32_e32 v114, s28, v114
	s_bcnt1_i32_b64 s28, s[22:23]
	v_mbcnt_lo_u32_b32 v111, s22, v114
	v_mbcnt_hi_u32_b32 v111, s23, v111
	v_add_u32_e32 v113, 0x201, v109
	v_lshl_add_u32 v112, v111, 2, s89
	s_mov_b64 exec, s[22:23]
	ds_write_b32 v112, v113
	s_mov_b64 exec, -1
	v_add_u32_e32 v114, s28, v114
	s_bcnt1_i32_b64 s28, s[24:25]
	v_mbcnt_lo_u32_b32 v111, s24, v114
	v_mbcnt_hi_u32_b32 v111, s25, v111
	v_add_u32_e32 v113, 0x202, v109
	v_lshl_add_u32 v112, v111, 2, s89
	s_mov_b64 exec, s[24:25]
	ds_write_b32 v112, v113
	s_mov_b64 exec, -1
	v_add_u32_e32 v114, s28, v114
	s_bcnt1_i32_b64 s28, s[26:27]
	v_mbcnt_lo_u32_b32 v111, s26, v114
	v_mbcnt_hi_u32_b32 v111, s27, v111
	v_add_u32_e32 v113, 0x203, v109
	v_lshl_add_u32 v112, v111, 2, s89
	s_mov_b64 exec, s[26:27]
	ds_write_b32 v112, v113
	s_mov_b64 exec, -1
	v_add_u32_e32 v114, s28, v114
	s_cmp_lt_u32 s0, 3
	s_cbranch_scc1 .Ltk_p1_done
	v_cmp_ge_u32_e64 s[20:21], v192, v110
	v_cmp_ge_u32_e64 s[22:23], v193, v110
	v_cmp_ge_u32_e64 s[24:25], v194, v110
	v_cmp_ge_u32_e64 s[26:27], v195, v110
	s_bcnt1_i32_b64 s28, s[20:21]
	v_mbcnt_lo_u32_b32 v111, s20, v114
	v_mbcnt_hi_u32_b32 v111, s21, v111
	v_add_u32_e32 v113, 0x300, v109
	v_lshl_add_u32 v112, v111, 2, s89
	s_mov_b64 exec, s[20:21]
	ds_write_b32 v112, v113
	s_mov_b64 exec, -1
	v_add_u32_e32 v114, s28, v114
	s_bcnt1_i32_b64 s28, s[22:23]
	v_mbcnt_lo_u32_b32 v111, s22, v114
	v_mbcnt_hi_u32_b32 v111, s23, v111
	v_add_u32_e32 v113, 0x301, v109
	v_lshl_add_u32 v112, v111, 2, s89
	s_mov_b64 exec, s[22:23]
	ds_write_b32 v112, v113
	s_mov_b64 exec, -1
	v_add_u32_e32 v114, s28, v114
	s_bcnt1_i32_b64 s28, s[24:25]
	v_mbcnt_lo_u32_b32 v111, s24, v114
	v_mbcnt_hi_u32_b32 v111, s25, v111
	v_add_u32_e32 v113, 0x302, v109
	v_lshl_add_u32 v112, v111, 2, s89
	s_mov_b64 exec, s[24:25]
	ds_write_b32 v112, v113
	s_mov_b64 exec, -1
	v_add_u32_e32 v114, s28, v114
	s_bcnt1_i32_b64 s28, s[26:27]
	v_mbcnt_lo_u32_b32 v111, s26, v114
	v_mbcnt_hi_u32_b32 v111, s27, v111
	v_add_u32_e32 v113, 0x303, v109
	v_lshl_add_u32 v112, v111, 2, s89
	s_mov_b64 exec, s[26:27]
	ds_write_b32 v112, v113
	s_mov_b64 exec, -1
	v_add_u32_e32 v114, s28, v114
	s_cmp_lt_u32 s0, 4
	s_cbranch_scc1 .Ltk_p1_done
	v_cmp_ge_u32_e64 s[20:21], v196, v110
	v_cmp_ge_u32_e64 s[22:23], v197, v110
	v_cmp_ge_u32_e64 s[24:25], v198, v110
	v_cmp_ge_u32_e64 s[26:27], v199, v110
	s_bcnt1_i32_b64 s28, s[20:21]
	v_mbcnt_lo_u32_b32 v111, s20, v114
	v_mbcnt_hi_u32_b32 v111, s21, v111
	v_add_u32_e32 v113, 0x400, v109
	v_lshl_add_u32 v112, v111, 2, s89
	s_mov_b64 exec, s[20:21]
	ds_write_b32 v112, v113
	s_mov_b64 exec, -1
	v_add_u32_e32 v114, s28, v114
	s_bcnt1_i32_b64 s28, s[22:23]
	v_mbcnt_lo_u32_b32 v111, s22, v114
	v_mbcnt_hi_u32_b32 v111, s23, v111
	v_add_u32_e32 v113, 0x401, v109
	v_lshl_add_u32 v112, v111, 2, s89
	s_mov_b64 exec, s[22:23]
	ds_write_b32 v112, v113
	s_mov_b64 exec, -1
	v_add_u32_e32 v114, s28, v114
	s_bcnt1_i32_b64 s28, s[24:25]
	v_mbcnt_lo_u32_b32 v111, s24, v114
	v_mbcnt_hi_u32_b32 v111, s25, v111
	v_add_u32_e32 v113, 0x402, v109
	v_lshl_add_u32 v112, v111, 2, s89
	s_mov_b64 exec, s[24:25]
	ds_write_b32 v112, v113
	s_mov_b64 exec, -1
	v_add_u32_e32 v114, s28, v114
	s_bcnt1_i32_b64 s28, s[26:27]
	v_mbcnt_lo_u32_b32 v111, s26, v114
	v_mbcnt_hi_u32_b32 v111, s27, v111
	v_add_u32_e32 v113, 0x403, v109
	v_lshl_add_u32 v112, v111, 2, s89
	s_mov_b64 exec, s[26:27]
	ds_write_b32 v112, v113
	s_mov_b64 exec, -1
	v_add_u32_e32 v114, s28, v114
	s_cmp_lt_u32 s0, 5
	s_cbranch_scc1 .Ltk_p1_done
	v_cmp_ge_u32_e64 s[20:21], v200, v110
	v_cmp_ge_u32_e64 s[22:23], v201, v110
	v_cmp_ge_u32_e64 s[24:25], v202, v110
	v_cmp_ge_u32_e64 s[26:27], v203, v110
	s_bcnt1_i32_b64 s28, s[20:21]
	v_mbcnt_lo_u32_b32 v111, s20, v114
	v_mbcnt_hi_u32_b32 v111, s21, v111
	v_add_u32_e32 v113, 0x500, v109
	v_lshl_add_u32 v112, v111, 2, s89
	s_mov_b64 exec, s[20:21]
	ds_write_b32 v112, v113
	s_mov_b64 exec, -1
	v_add_u32_e32 v114, s28, v114
	s_bcnt1_i32_b64 s28, s[22:23]
	v_mbcnt_lo_u32_b32 v111, s22, v114
	v_mbcnt_hi_u32_b32 v111, s23, v111
	v_add_u32_e32 v113, 0x501, v109
	v_lshl_add_u32 v112, v111, 2, s89
	s_mov_b64 exec, s[22:23]
	ds_write_b32 v112, v113
	s_mov_b64 exec, -1
	v_add_u32_e32 v114, s28, v114
	s_bcnt1_i32_b64 s28, s[24:25]
	v_mbcnt_lo_u32_b32 v111, s24, v114
	v_mbcnt_hi_u32_b32 v111, s25, v111
	v_add_u32_e32 v113, 0x502, v109
	v_lshl_add_u32 v112, v111, 2, s89
	s_mov_b64 exec, s[24:25]
	ds_write_b32 v112, v113
	s_mov_b64 exec, -1
	v_add_u32_e32 v114, s28, v114
	s_bcnt1_i32_b64 s28, s[26:27]
	v_mbcnt_lo_u32_b32 v111, s26, v114
	v_mbcnt_hi_u32_b32 v111, s27, v111
	v_add_u32_e32 v113, 0x503, v109
	v_lshl_add_u32 v112, v111, 2, s89
	s_mov_b64 exec, s[26:27]
	ds_write_b32 v112, v113
	s_mov_b64 exec, -1
	v_add_u32_e32 v114, s28, v114
	s_cmp_lt_u32 s0, 6
	s_cbranch_scc1 .Ltk_p1_done
	v_cmp_ge_u32_e64 s[20:21], v204, v110
	v_cmp_ge_u32_e64 s[22:23], v205, v110
	v_cmp_ge_u32_e64 s[24:25], v206, v110
	v_cmp_ge_u32_e64 s[26:27], v207, v110
	s_bcnt1_i32_b64 s28, s[20:21]
	v_mbcnt_lo_u32_b32 v111, s20, v114
	v_mbcnt_hi_u32_b32 v111, s21, v111
	v_add_u32_e32 v113, 0x600, v109
	v_lshl_add_u32 v112, v111, 2, s89
	s_mov_b64 exec, s[20:21]
	ds_write_b32 v112, v113
	s_mov_b64 exec, -1
	v_add_u32_e32 v114, s28, v114
	s_bcnt1_i32_b64 s28, s[22:23]
	v_mbcnt_lo_u32_b32 v111, s22, v114
	v_mbcnt_hi_u32_b32 v111, s23, v111
	v_add_u32_e32 v113, 0x601, v109
	v_lshl_add_u32 v112, v111, 2, s89
	s_mov_b64 exec, s[22:23]
	ds_write_b32 v112, v113
	s_mov_b64 exec, -1
	v_add_u32_e32 v114, s28, v114
	s_bcnt1_i32_b64 s28, s[24:25]
	v_mbcnt_lo_u32_b32 v111, s24, v114
	v_mbcnt_hi_u32_b32 v111, s25, v111
	v_add_u32_e32 v113, 0x602, v109
	v_lshl_add_u32 v112, v111, 2, s89
	s_mov_b64 exec, s[24:25]
	ds_write_b32 v112, v113
	s_mov_b64 exec, -1
	v_add_u32_e32 v114, s28, v114
	s_bcnt1_i32_b64 s28, s[26:27]
	v_mbcnt_lo_u32_b32 v111, s26, v114
	v_mbcnt_hi_u32_b32 v111, s27, v111
	v_add_u32_e32 v113, 0x603, v109
	v_lshl_add_u32 v112, v111, 2, s89
	s_mov_b64 exec, s[26:27]
	ds_write_b32 v112, v113
	s_mov_b64 exec, -1
	v_add_u32_e32 v114, s28, v114
	s_cmp_lt_u32 s0, 7
	s_cbranch_scc1 .Ltk_p1_done
	v_cmp_ge_u32_e64 s[20:21], v208, v110
	v_cmp_ge_u32_e64 s[22:23], v209, v110
	v_cmp_ge_u32_e64 s[24:25], v210, v110
	v_cmp_ge_u32_e64 s[26:27], v211, v110
	s_bcnt1_i32_b64 s28, s[20:21]
	v_mbcnt_lo_u32_b32 v111, s20, v114
	v_mbcnt_hi_u32_b32 v111, s21, v111
	v_add_u32_e32 v113, 0x700, v109
	v_lshl_add_u32 v112, v111, 2, s89
	s_mov_b64 exec, s[20:21]
	ds_write_b32 v112, v113
	s_mov_b64 exec, -1
	v_add_u32_e32 v114, s28, v114
	s_bcnt1_i32_b64 s28, s[22:23]
	v_mbcnt_lo_u32_b32 v111, s22, v114
	v_mbcnt_hi_u32_b32 v111, s23, v111
	v_add_u32_e32 v113, 0x701, v109
	v_lshl_add_u32 v112, v111, 2, s89
	s_mov_b64 exec, s[22:23]
	ds_write_b32 v112, v113
	s_mov_b64 exec, -1
	v_add_u32_e32 v114, s28, v114
	s_bcnt1_i32_b64 s28, s[24:25]
	v_mbcnt_lo_u32_b32 v111, s24, v114
	v_mbcnt_hi_u32_b32 v111, s25, v111
	v_add_u32_e32 v113, 0x702, v109
	v_lshl_add_u32 v112, v111, 2, s89
	s_mov_b64 exec, s[24:25]
	ds_write_b32 v112, v113
	s_mov_b64 exec, -1
	v_add_u32_e32 v114, s28, v114
	s_bcnt1_i32_b64 s28, s[26:27]
	v_mbcnt_lo_u32_b32 v111, s26, v114
	v_mbcnt_hi_u32_b32 v111, s27, v111
	v_add_u32_e32 v113, 0x703, v109
	v_lshl_add_u32 v112, v111, 2, s89
	s_mov_b64 exec, s[26:27]
	ds_write_b32 v112, v113
	s_mov_b64 exec, -1
	v_add_u32_e32 v114, s28, v114
	s_cmp_lt_u32 s0, 8
	s_cbranch_scc1 .Ltk_p1_done
	v_cmp_ge_u32_e64 s[20:21], v212, v110
	v_cmp_ge_u32_e64 s[22:23], v213, v110
	v_cmp_ge_u32_e64 s[24:25], v214, v110
	v_cmp_ge_u32_e64 s[26:27], v215, v110
	s_bcnt1_i32_b64 s28, s[20:21]
	v_mbcnt_lo_u32_b32 v111, s20, v114
	v_mbcnt_hi_u32_b32 v111, s21, v111
	v_add_u32_e32 v113, 0x800, v109
	v_lshl_add_u32 v112, v111, 2, s89
	s_mov_b64 exec, s[20:21]
	ds_write_b32 v112, v113
	s_mov_b64 exec, -1
	v_add_u32_e32 v114, s28, v114
	s_bcnt1_i32_b64 s28, s[22:23]
	v_mbcnt_lo_u32_b32 v111, s22, v114
	v_mbcnt_hi_u32_b32 v111, s23, v111
	v_add_u32_e32 v113, 0x801, v109
	v_lshl_add_u32 v112, v111, 2, s89
	s_mov_b64 exec, s[22:23]
	ds_write_b32 v112, v113
	s_mov_b64 exec, -1
	v_add_u32_e32 v114, s28, v114
	s_bcnt1_i32_b64 s28, s[24:25]
	v_mbcnt_lo_u32_b32 v111, s24, v114
	v_mbcnt_hi_u32_b32 v111, s25, v111
	v_add_u32_e32 v113, 0x802, v109
	v_lshl_add_u32 v112, v111, 2, s89
	s_mov_b64 exec, s[24:25]
	ds_write_b32 v112, v113
	s_mov_b64 exec, -1
	v_add_u32_e32 v114, s28, v114
	s_bcnt1_i32_b64 s28, s[26:27]
	v_mbcnt_lo_u32_b32 v111, s26, v114
	v_mbcnt_hi_u32_b32 v111, s27, v111
	v_add_u32_e32 v113, 0x803, v109
	v_lshl_add_u32 v112, v111, 2, s89
	s_mov_b64 exec, s[26:27]
	ds_write_b32 v112, v113
	s_mov_b64 exec, -1
	v_add_u32_e32 v114, s28, v114
	s_cmp_lt_u32 s0, 9
	s_cbranch_scc1 .Ltk_p1_done
	v_cmp_ge_u32_e64 s[20:21], v216, v110
	v_cmp_ge_u32_e64 s[22:23], v217, v110
	v_cmp_ge_u32_e64 s[24:25], v218, v110
	v_cmp_ge_u32_e64 s[26:27], v219, v110
	s_bcnt1_i32_b64 s28, s[20:21]
	v_mbcnt_lo_u32_b32 v111, s20, v114
	v_mbcnt_hi_u32_b32 v111, s21, v111
	v_add_u32_e32 v113, 0x900, v109
	v_lshl_add_u32 v112, v111, 2, s89
	s_mov_b64 exec, s[20:21]
	ds_write_b32 v112, v113
	s_mov_b64 exec, -1
	v_add_u32_e32 v114, s28, v114
	s_bcnt1_i32_b64 s28, s[22:23]
	v_mbcnt_lo_u32_b32 v111, s22, v114
	v_mbcnt_hi_u32_b32 v111, s23, v111
	v_add_u32_e32 v113, 0x901, v109
	v_lshl_add_u32 v112, v111, 2, s89
	s_mov_b64 exec, s[22:23]
	ds_write_b32 v112, v113
	s_mov_b64 exec, -1
	v_add_u32_e32 v114, s28, v114
	s_bcnt1_i32_b64 s28, s[24:25]
	v_mbcnt_lo_u32_b32 v111, s24, v114
	v_mbcnt_hi_u32_b32 v111, s25, v111
	v_add_u32_e32 v113, 0x902, v109
	v_lshl_add_u32 v112, v111, 2, s89
	s_mov_b64 exec, s[24:25]
	ds_write_b32 v112, v113
	s_mov_b64 exec, -1
	v_add_u32_e32 v114, s28, v114
	s_bcnt1_i32_b64 s28, s[26:27]
	v_mbcnt_lo_u32_b32 v111, s26, v114
	v_mbcnt_hi_u32_b32 v111, s27, v111
	v_add_u32_e32 v113, 0x903, v109
	v_lshl_add_u32 v112, v111, 2, s89
	s_mov_b64 exec, s[26:27]
	ds_write_b32 v112, v113
	s_mov_b64 exec, -1
	v_add_u32_e32 v114, s28, v114
	s_cmp_lt_u32 s0, 10
	s_cbranch_scc1 .Ltk_p1_done
	v_cmp_ge_u32_e64 s[20:21], v220, v110
	v_cmp_ge_u32_e64 s[22:23], v221, v110
	v_cmp_ge_u32_e64 s[24:25], v222, v110
	v_cmp_ge_u32_e64 s[26:27], v223, v110
	s_bcnt1_i32_b64 s28, s[20:21]
	v_mbcnt_lo_u32_b32 v111, s20, v114
	v_mbcnt_hi_u32_b32 v111, s21, v111
	v_add_u32_e32 v113, 0xa00, v109
	v_lshl_add_u32 v112, v111, 2, s89
	s_mov_b64 exec, s[20:21]
	ds_write_b32 v112, v113
	s_mov_b64 exec, -1
	v_add_u32_e32 v114, s28, v114
	s_bcnt1_i32_b64 s28, s[22:23]
	v_mbcnt_lo_u32_b32 v111, s22, v114
	v_mbcnt_hi_u32_b32 v111, s23, v111
	v_add_u32_e32 v113, 0xa01, v109
	v_lshl_add_u32 v112, v111, 2, s89
	s_mov_b64 exec, s[22:23]
	ds_write_b32 v112, v113
	s_mov_b64 exec, -1
	v_add_u32_e32 v114, s28, v114
	s_bcnt1_i32_b64 s28, s[24:25]
	v_mbcnt_lo_u32_b32 v111, s24, v114
	v_mbcnt_hi_u32_b32 v111, s25, v111
	v_add_u32_e32 v113, 0xa02, v109
	v_lshl_add_u32 v112, v111, 2, s89
	s_mov_b64 exec, s[24:25]
	ds_write_b32 v112, v113
	s_mov_b64 exec, -1
	v_add_u32_e32 v114, s28, v114
	s_bcnt1_i32_b64 s28, s[26:27]
	v_mbcnt_lo_u32_b32 v111, s26, v114
	v_mbcnt_hi_u32_b32 v111, s27, v111
	v_add_u32_e32 v113, 0xa03, v109
	v_lshl_add_u32 v112, v111, 2, s89
	s_mov_b64 exec, s[26:27]
	ds_write_b32 v112, v113
	s_mov_b64 exec, -1
	v_add_u32_e32 v114, s28, v114
	s_cmp_lt_u32 s0, 11
	s_cbranch_scc1 .Ltk_p1_done
	v_cmp_ge_u32_e64 s[20:21], v224, v110
	v_cmp_ge_u32_e64 s[22:23], v225, v110
	v_cmp_ge_u32_e64 s[24:25], v226, v110
	v_cmp_ge_u32_e64 s[26:27], v227, v110
	s_bcnt1_i32_b64 s28, s[20:21]
	v_mbcnt_lo_u32_b32 v111, s20, v114
	v_mbcnt_hi_u32_b32 v111, s21, v111
	v_add_u32_e32 v113, 0xb00, v109
	v_lshl_add_u32 v112, v111, 2, s89
	s_mov_b64 exec, s[20:21]
	ds_write_b32 v112, v113
	s_mov_b64 exec, -1
	v_add_u32_e32 v114, s28, v114
	s_bcnt1_i32_b64 s28, s[22:23]
	v_mbcnt_lo_u32_b32 v111, s22, v114
	v_mbcnt_hi_u32_b32 v111, s23, v111
	v_add_u32_e32 v113, 0xb01, v109
	v_lshl_add_u32 v112, v111, 2, s89
	s_mov_b64 exec, s[22:23]
	ds_write_b32 v112, v113
	s_mov_b64 exec, -1
	v_add_u32_e32 v114, s28, v114
	s_bcnt1_i32_b64 s28, s[24:25]
	v_mbcnt_lo_u32_b32 v111, s24, v114
	v_mbcnt_hi_u32_b32 v111, s25, v111
	v_add_u32_e32 v113, 0xb02, v109
	v_lshl_add_u32 v112, v111, 2, s89
	s_mov_b64 exec, s[24:25]
	ds_write_b32 v112, v113
	s_mov_b64 exec, -1
	v_add_u32_e32 v114, s28, v114
	s_bcnt1_i32_b64 s28, s[26:27]
	v_mbcnt_lo_u32_b32 v111, s26, v114
	v_mbcnt_hi_u32_b32 v111, s27, v111
	v_add_u32_e32 v113, 0xb03, v109
	v_lshl_add_u32 v112, v111, 2, s89
	s_mov_b64 exec, s[26:27]
	ds_write_b32 v112, v113
	s_mov_b64 exec, -1
	v_add_u32_e32 v114, s28, v114
	s_cmp_lt_u32 s0, 12
	s_cbranch_scc1 .Ltk_p1_done
	v_cmp_ge_u32_e64 s[20:21], v228, v110
	v_cmp_ge_u32_e64 s[22:23], v229, v110
	v_cmp_ge_u32_e64 s[24:25], v230, v110
	v_cmp_ge_u32_e64 s[26:27], v231, v110
	s_bcnt1_i32_b64 s28, s[20:21]
	v_mbcnt_lo_u32_b32 v111, s20, v114
	v_mbcnt_hi_u32_b32 v111, s21, v111
	v_add_u32_e32 v113, 0xc00, v109
	v_lshl_add_u32 v112, v111, 2, s89
	s_mov_b64 exec, s[20:21]
	ds_write_b32 v112, v113
	s_mov_b64 exec, -1
	v_add_u32_e32 v114, s28, v114
	s_bcnt1_i32_b64 s28, s[22:23]
	v_mbcnt_lo_u32_b32 v111, s22, v114
	v_mbcnt_hi_u32_b32 v111, s23, v111
	v_add_u32_e32 v113, 0xc01, v109
	v_lshl_add_u32 v112, v111, 2, s89
	s_mov_b64 exec, s[22:23]
	ds_write_b32 v112, v113
	s_mov_b64 exec, -1
	v_add_u32_e32 v114, s28, v114
	s_bcnt1_i32_b64 s28, s[24:25]
	v_mbcnt_lo_u32_b32 v111, s24, v114
	v_mbcnt_hi_u32_b32 v111, s25, v111
	v_add_u32_e32 v113, 0xc02, v109
	v_lshl_add_u32 v112, v111, 2, s89
	s_mov_b64 exec, s[24:25]
	ds_write_b32 v112, v113
	s_mov_b64 exec, -1
	v_add_u32_e32 v114, s28, v114
	s_bcnt1_i32_b64 s28, s[26:27]
	v_mbcnt_lo_u32_b32 v111, s26, v114
	v_mbcnt_hi_u32_b32 v111, s27, v111
	v_add_u32_e32 v113, 0xc03, v109
	v_lshl_add_u32 v112, v111, 2, s89
	s_mov_b64 exec, s[26:27]
	ds_write_b32 v112, v113
	s_mov_b64 exec, -1
	v_add_u32_e32 v114, s28, v114
	s_cmp_lt_u32 s0, 13
	s_cbranch_scc1 .Ltk_p1_done
	v_cmp_ge_u32_e64 s[20:21], v232, v110
	v_cmp_ge_u32_e64 s[22:23], v233, v110
	v_cmp_ge_u32_e64 s[24:25], v234, v110
	v_cmp_ge_u32_e64 s[26:27], v235, v110
	s_bcnt1_i32_b64 s28, s[20:21]
	v_mbcnt_lo_u32_b32 v111, s20, v114
	v_mbcnt_hi_u32_b32 v111, s21, v111
	v_add_u32_e32 v113, 0xd00, v109
	v_lshl_add_u32 v112, v111, 2, s89
	s_mov_b64 exec, s[20:21]
	ds_write_b32 v112, v113
	s_mov_b64 exec, -1
	v_add_u32_e32 v114, s28, v114
	s_bcnt1_i32_b64 s28, s[22:23]
	v_mbcnt_lo_u32_b32 v111, s22, v114
	v_mbcnt_hi_u32_b32 v111, s23, v111
	v_add_u32_e32 v113, 0xd01, v109
	v_lshl_add_u32 v112, v111, 2, s89
	s_mov_b64 exec, s[22:23]
	ds_write_b32 v112, v113
	s_mov_b64 exec, -1
	v_add_u32_e32 v114, s28, v114
	s_bcnt1_i32_b64 s28, s[24:25]
	v_mbcnt_lo_u32_b32 v111, s24, v114
	v_mbcnt_hi_u32_b32 v111, s25, v111
	v_add_u32_e32 v113, 0xd02, v109
	v_lshl_add_u32 v112, v111, 2, s89
	s_mov_b64 exec, s[24:25]
	ds_write_b32 v112, v113
	s_mov_b64 exec, -1
	v_add_u32_e32 v114, s28, v114
	s_bcnt1_i32_b64 s28, s[26:27]
	v_mbcnt_lo_u32_b32 v111, s26, v114
	v_mbcnt_hi_u32_b32 v111, s27, v111
	v_add_u32_e32 v113, 0xd03, v109
	v_lshl_add_u32 v112, v111, 2, s89
	s_mov_b64 exec, s[26:27]
	ds_write_b32 v112, v113
	s_mov_b64 exec, -1
	v_add_u32_e32 v114, s28, v114
	s_cmp_lt_u32 s0, 14
	s_cbranch_scc1 .Ltk_p1_done
	v_cmp_ge_u32_e64 s[20:21], v236, v110
	v_cmp_ge_u32_e64 s[22:23], v237, v110
	v_cmp_ge_u32_e64 s[24:25], v238, v110
	v_cmp_ge_u32_e64 s[26:27], v239, v110
	s_bcnt1_i32_b64 s28, s[20:21]
	v_mbcnt_lo_u32_b32 v111, s20, v114
	v_mbcnt_hi_u32_b32 v111, s21, v111
	v_add_u32_e32 v113, 0xe00, v109
	v_lshl_add_u32 v112, v111, 2, s89
	s_mov_b64 exec, s[20:21]
	ds_write_b32 v112, v113
	s_mov_b64 exec, -1
	v_add_u32_e32 v114, s28, v114
	s_bcnt1_i32_b64 s28, s[22:23]
	v_mbcnt_lo_u32_b32 v111, s22, v114
	v_mbcnt_hi_u32_b32 v111, s23, v111
	v_add_u32_e32 v113, 0xe01, v109
	v_lshl_add_u32 v112, v111, 2, s89
	s_mov_b64 exec, s[22:23]
	ds_write_b32 v112, v113
	s_mov_b64 exec, -1
	v_add_u32_e32 v114, s28, v114
	s_bcnt1_i32_b64 s28, s[24:25]
	v_mbcnt_lo_u32_b32 v111, s24, v114
	v_mbcnt_hi_u32_b32 v111, s25, v111
	v_add_u32_e32 v113, 0xe02, v109
	v_lshl_add_u32 v112, v111, 2, s89
	s_mov_b64 exec, s[24:25]
	ds_write_b32 v112, v113
	s_mov_b64 exec, -1
	v_add_u32_e32 v114, s28, v114
	s_bcnt1_i32_b64 s28, s[26:27]
	v_mbcnt_lo_u32_b32 v111, s26, v114
	v_mbcnt_hi_u32_b32 v111, s27, v111
	v_add_u32_e32 v113, 0xe03, v109
	v_lshl_add_u32 v112, v111, 2, s89
	s_mov_b64 exec, s[26:27]
	ds_write_b32 v112, v113
	s_mov_b64 exec, -1
	v_add_u32_e32 v114, s28, v114
	s_cmp_lt_u32 s0, 15
	s_cbranch_scc1 .Ltk_p1_done
	v_cmp_ge_u32_e64 s[20:21], v134, v110
	v_cmp_ge_u32_e64 s[22:23], v135, v110
	v_cmp_ge_u32_e64 s[24:25], v136, v110
	v_cmp_ge_u32_e64 s[26:27], v137, v110
	s_bcnt1_i32_b64 s28, s[20:21]
	v_mbcnt_lo_u32_b32 v111, s20, v114
	v_mbcnt_hi_u32_b32 v111, s21, v111
	v_add_u32_e32 v113, 0xf00, v109
	v_lshl_add_u32 v112, v111, 2, s89
	s_mov_b64 exec, s[20:21]
	ds_write_b32 v112, v113
	s_mov_b64 exec, -1
	v_add_u32_e32 v114, s28, v114
	s_bcnt1_i32_b64 s28, s[22:23]
	v_mbcnt_lo_u32_b32 v111, s22, v114
	v_mbcnt_hi_u32_b32 v111, s23, v111
	v_add_u32_e32 v113, 0xf01, v109
	v_lshl_add_u32 v112, v111, 2, s89
	s_mov_b64 exec, s[22:23]
	ds_write_b32 v112, v113
	s_mov_b64 exec, -1
	v_add_u32_e32 v114, s28, v114
	s_bcnt1_i32_b64 s28, s[24:25]
	v_mbcnt_lo_u32_b32 v111, s24, v114
	v_mbcnt_hi_u32_b32 v111, s25, v111
	v_add_u32_e32 v113, 0xf02, v109
	v_lshl_add_u32 v112, v111, 2, s89
	s_mov_b64 exec, s[24:25]
	ds_write_b32 v112, v113
	s_mov_b64 exec, -1
	v_add_u32_e32 v114, s28, v114
	s_bcnt1_i32_b64 s28, s[26:27]
	v_mbcnt_lo_u32_b32 v111, s26, v114
	v_mbcnt_hi_u32_b32 v111, s27, v111
	v_add_u32_e32 v113, 0xf03, v109
	v_lshl_add_u32 v112, v111, 2, s89
	s_mov_b64 exec, s[26:27]
	ds_write_b32 v112, v113
	s_mov_b64 exec, -1
	v_add_u32_e32 v114, s28, v114
.Ltk_p1_done:
	s_cmp_lg_u32 s10, 0
	s_cbranch_scc1 .Ltk_fin
	v_mov_b32_e32 v110, s11
	v_cmp_eq_u32_e64 s[20:21], v180, v110
	v_cmp_eq_u32_e64 s[22:23], v181, v110
	v_cmp_eq_u32_e64 s[24:25], v182, v110
	v_cmp_eq_u32_e64 s[26:27], v183, v110
	s_bcnt1_i32_b64 s28, s[20:21]
	v_mbcnt_lo_u32_b32 v111, s20, v114
	v_mbcnt_hi_u32_b32 v111, s21, v111
	v_add_u32_e32 v113, 0, v109
	v_lshl_add_u32 v112, v111, 2, s89
	v_cmp_gt_u32_e64 s[36:37], s29, v111
	s_nop 0
	s_and_b64 s[36:37], s[36:37], s[20:21]
	s_mov_b64 exec, s[36:37]
	ds_write_b32 v112, v113
	s_mov_b64 exec, -1
	v_add_u32_e32 v114, s28, v114
	s_bcnt1_i32_b64 s28, s[22:23]
	v_mbcnt_lo_u32_b32 v111, s22, v114
	v_mbcnt_hi_u32_b32 v111, s23, v111
	v_add_u32_e32 v113, 1, v109
	v_lshl_add_u32 v112, v111, 2, s89
	v_cmp_gt_u32_e64 s[36:37], s29, v111
	s_nop 0
	s_and_b64 s[36:37], s[36:37], s[22:23]
	s_mov_b64 exec, s[36:37]
	ds_write_b32 v112, v113
	s_mov_b64 exec, -1
	v_add_u32_e32 v114, s28, v114
	s_bcnt1_i32_b64 s28, s[24:25]
	v_mbcnt_lo_u32_b32 v111, s24, v114
	v_mbcnt_hi_u32_b32 v111, s25, v111
	v_add_u32_e32 v113, 2, v109
	v_lshl_add_u32 v112, v111, 2, s89
	v_cmp_gt_u32_e64 s[36:37], s29, v111
	s_nop 0
	s_and_b64 s[36:37], s[36:37], s[24:25]
	s_mov_b64 exec, s[36:37]
	ds_write_b32 v112, v113
	s_mov_b64 exec, -1
	v_add_u32_e32 v114, s28, v114
	s_bcnt1_i32_b64 s28, s[26:27]
	v_mbcnt_lo_u32_b32 v111, s26, v114
	v_mbcnt_hi_u32_b32 v111, s27, v111
	v_add_u32_e32 v113, 3, v109
	v_lshl_add_u32 v112, v111, 2, s89
	v_cmp_gt_u32_e64 s[36:37], s29, v111
	s_nop 0
	s_and_b64 s[36:37], s[36:37], s[26:27]
	s_mov_b64 exec, s[36:37]
	ds_write_b32 v112, v113
	s_mov_b64 exec, -1
	v_add_u32_e32 v114, s28, v114
	v_cmp_eq_u32_e64 s[20:21], v184, v110
	v_cmp_eq_u32_e64 s[22:23], v185, v110
	v_cmp_eq_u32_e64 s[24:25], v186, v110
	v_cmp_eq_u32_e64 s[26:27], v187, v110
	s_bcnt1_i32_b64 s28, s[20:21]
	v_mbcnt_lo_u32_b32 v111, s20, v114
	v_mbcnt_hi_u32_b32 v111, s21, v111
	v_add_u32_e32 v113, 0x100, v109
	v_lshl_add_u32 v112, v111, 2, s89
	v_cmp_gt_u32_e64 s[36:37], s29, v111
	s_nop 0
	s_and_b64 s[36:37], s[36:37], s[20:21]
	s_mov_b64 exec, s[36:37]
	ds_write_b32 v112, v113
	s_mov_b64 exec, -1
	v_add_u32_e32 v114, s28, v114
	s_bcnt1_i32_b64 s28, s[22:23]
	v_mbcnt_lo_u32_b32 v111, s22, v114
	v_mbcnt_hi_u32_b32 v111, s23, v111
	v_add_u32_e32 v113, 0x101, v109
	v_lshl_add_u32 v112, v111, 2, s89
	v_cmp_gt_u32_e64 s[36:37], s29, v111
	s_nop 0
	s_and_b64 s[36:37], s[36:37], s[22:23]
	s_mov_b64 exec, s[36:37]
	ds_write_b32 v112, v113
	s_mov_b64 exec, -1
	v_add_u32_e32 v114, s28, v114
	s_bcnt1_i32_b64 s28, s[24:25]
	v_mbcnt_lo_u32_b32 v111, s24, v114
	v_mbcnt_hi_u32_b32 v111, s25, v111
	v_add_u32_e32 v113, 0x102, v109
	v_lshl_add_u32 v112, v111, 2, s89
	v_cmp_gt_u32_e64 s[36:37], s29, v111
	s_nop 0
	s_and_b64 s[36:37], s[36:37], s[24:25]
	s_mov_b64 exec, s[36:37]
	ds_write_b32 v112, v113
	s_mov_b64 exec, -1
	v_add_u32_e32 v114, s28, v114
	s_bcnt1_i32_b64 s28, s[26:27]
	v_mbcnt_lo_u32_b32 v111, s26, v114
	v_mbcnt_hi_u32_b32 v111, s27, v111
	v_add_u32_e32 v113, 0x103, v109
	v_lshl_add_u32 v112, v111, 2, s89
	v_cmp_gt_u32_e64 s[36:37], s29, v111
	s_nop 0
	s_and_b64 s[36:37], s[36:37], s[26:27]
	s_mov_b64 exec, s[36:37]
	ds_write_b32 v112, v113
	s_mov_b64 exec, -1
	v_add_u32_e32 v114, s28, v114
	s_cmp_lt_u32 s0, 2
	s_cbranch_scc1 .Ltk_p2_done
	v_cmp_eq_u32_e64 s[20:21], v188, v110
	v_cmp_eq_u32_e64 s[22:23], v189, v110
	v_cmp_eq_u32_e64 s[24:25], v190, v110
	v_cmp_eq_u32_e64 s[26:27], v191, v110
	s_bcnt1_i32_b64 s28, s[20:21]
	v_mbcnt_lo_u32_b32 v111, s20, v114
	v_mbcnt_hi_u32_b32 v111, s21, v111
	v_add_u32_e32 v113, 0x200, v109
	v_lshl_add_u32 v112, v111, 2, s89
	v_cmp_gt_u32_e64 s[36:37], s29, v111
	s_nop 0
	s_and_b64 s[36:37], s[36:37], s[20:21]
	s_mov_b64 exec, s[36:37]
	ds_write_b32 v112, v113
	s_mov_b64 exec, -1
	v_add_u32_e32 v114, s28, v114
	s_bcnt1_i32_b64 s28, s[22:23]
	v_mbcnt_lo_u32_b32 v111, s22, v114
	v_mbcnt_hi_u32_b32 v111, s23, v111
	v_add_u32_e32 v113, 0x201, v109
	v_lshl_add_u32 v112, v111, 2, s89
	v_cmp_gt_u32_e64 s[36:37], s29, v111
	s_nop 0
	s_and_b64 s[36:37], s[36:37], s[22:23]
	s_mov_b64 exec, s[36:37]
	ds_write_b32 v112, v113
	s_mov_b64 exec, -1
	v_add_u32_e32 v114, s28, v114
	s_bcnt1_i32_b64 s28, s[24:25]
	v_mbcnt_lo_u32_b32 v111, s24, v114
	v_mbcnt_hi_u32_b32 v111, s25, v111
	v_add_u32_e32 v113, 0x202, v109
	v_lshl_add_u32 v112, v111, 2, s89
	v_cmp_gt_u32_e64 s[36:37], s29, v111
	s_nop 0
	s_and_b64 s[36:37], s[36:37], s[24:25]
	s_mov_b64 exec, s[36:37]
	ds_write_b32 v112, v113
	s_mov_b64 exec, -1
	v_add_u32_e32 v114, s28, v114
	s_bcnt1_i32_b64 s28, s[26:27]
	v_mbcnt_lo_u32_b32 v111, s26, v114
	v_mbcnt_hi_u32_b32 v111, s27, v111
	v_add_u32_e32 v113, 0x203, v109
	v_lshl_add_u32 v112, v111, 2, s89
	v_cmp_gt_u32_e64 s[36:37], s29, v111
	s_nop 0
	s_and_b64 s[36:37], s[36:37], s[26:27]
	s_mov_b64 exec, s[36:37]
	ds_write_b32 v112, v113
	s_mov_b64 exec, -1
	v_add_u32_e32 v114, s28, v114
	s_cmp_lt_u32 s0, 3
	s_cbranch_scc1 .Ltk_p2_done
	v_cmp_eq_u32_e64 s[20:21], v192, v110
	v_cmp_eq_u32_e64 s[22:23], v193, v110
	v_cmp_eq_u32_e64 s[24:25], v194, v110
	v_cmp_eq_u32_e64 s[26:27], v195, v110
	s_bcnt1_i32_b64 s28, s[20:21]
	v_mbcnt_lo_u32_b32 v111, s20, v114
	v_mbcnt_hi_u32_b32 v111, s21, v111
	v_add_u32_e32 v113, 0x300, v109
	v_lshl_add_u32 v112, v111, 2, s89
	v_cmp_gt_u32_e64 s[36:37], s29, v111
	s_nop 0
	s_and_b64 s[36:37], s[36:37], s[20:21]
	s_mov_b64 exec, s[36:37]
	ds_write_b32 v112, v113
	s_mov_b64 exec, -1
	v_add_u32_e32 v114, s28, v114
	s_bcnt1_i32_b64 s28, s[22:23]
	v_mbcnt_lo_u32_b32 v111, s22, v114
	v_mbcnt_hi_u32_b32 v111, s23, v111
	v_add_u32_e32 v113, 0x301, v109
	v_lshl_add_u32 v112, v111, 2, s89
	v_cmp_gt_u32_e64 s[36:37], s29, v111
	s_nop 0
	s_and_b64 s[36:37], s[36:37], s[22:23]
	s_mov_b64 exec, s[36:37]
	ds_write_b32 v112, v113
	s_mov_b64 exec, -1
	v_add_u32_e32 v114, s28, v114
	s_bcnt1_i32_b64 s28, s[24:25]
	v_mbcnt_lo_u32_b32 v111, s24, v114
	v_mbcnt_hi_u32_b32 v111, s25, v111
	v_add_u32_e32 v113, 0x302, v109
	v_lshl_add_u32 v112, v111, 2, s89
	v_cmp_gt_u32_e64 s[36:37], s29, v111
	s_nop 0
	s_and_b64 s[36:37], s[36:37], s[24:25]
	s_mov_b64 exec, s[36:37]
	ds_write_b32 v112, v113
	s_mov_b64 exec, -1
	v_add_u32_e32 v114, s28, v114
	s_bcnt1_i32_b64 s28, s[26:27]
	v_mbcnt_lo_u32_b32 v111, s26, v114
	v_mbcnt_hi_u32_b32 v111, s27, v111
	v_add_u32_e32 v113, 0x303, v109
	v_lshl_add_u32 v112, v111, 2, s89
	v_cmp_gt_u32_e64 s[36:37], s29, v111
	s_nop 0
	s_and_b64 s[36:37], s[36:37], s[26:27]
	s_mov_b64 exec, s[36:37]
	ds_write_b32 v112, v113
	s_mov_b64 exec, -1
	v_add_u32_e32 v114, s28, v114
	s_cmp_lt_u32 s0, 4
	s_cbranch_scc1 .Ltk_p2_done
	v_cmp_eq_u32_e64 s[20:21], v196, v110
	v_cmp_eq_u32_e64 s[22:23], v197, v110
	v_cmp_eq_u32_e64 s[24:25], v198, v110
	v_cmp_eq_u32_e64 s[26:27], v199, v110
	s_bcnt1_i32_b64 s28, s[20:21]
	v_mbcnt_lo_u32_b32 v111, s20, v114
	v_mbcnt_hi_u32_b32 v111, s21, v111
	v_add_u32_e32 v113, 0x400, v109
	v_lshl_add_u32 v112, v111, 2, s89
	v_cmp_gt_u32_e64 s[36:37], s29, v111
	s_nop 0
	s_and_b64 s[36:37], s[36:37], s[20:21]
	s_mov_b64 exec, s[36:37]
	ds_write_b32 v112, v113
	s_mov_b64 exec, -1
	v_add_u32_e32 v114, s28, v114
	s_bcnt1_i32_b64 s28, s[22:23]
	v_mbcnt_lo_u32_b32 v111, s22, v114
	v_mbcnt_hi_u32_b32 v111, s23, v111
	v_add_u32_e32 v113, 0x401, v109
	v_lshl_add_u32 v112, v111, 2, s89
	v_cmp_gt_u32_e64 s[36:37], s29, v111
	s_nop 0
	s_and_b64 s[36:37], s[36:37], s[22:23]
	s_mov_b64 exec, s[36:37]
	ds_write_b32 v112, v113
	s_mov_b64 exec, -1
	v_add_u32_e32 v114, s28, v114
	s_bcnt1_i32_b64 s28, s[24:25]
	v_mbcnt_lo_u32_b32 v111, s24, v114
	v_mbcnt_hi_u32_b32 v111, s25, v111
	v_add_u32_e32 v113, 0x402, v109
	v_lshl_add_u32 v112, v111, 2, s89
	v_cmp_gt_u32_e64 s[36:37], s29, v111
	s_nop 0
	s_and_b64 s[36:37], s[36:37], s[24:25]
	s_mov_b64 exec, s[36:37]
	ds_write_b32 v112, v113
	s_mov_b64 exec, -1
	v_add_u32_e32 v114, s28, v114
	s_bcnt1_i32_b64 s28, s[26:27]
	v_mbcnt_lo_u32_b32 v111, s26, v114
	v_mbcnt_hi_u32_b32 v111, s27, v111
	v_add_u32_e32 v113, 0x403, v109
	v_lshl_add_u32 v112, v111, 2, s89
	v_cmp_gt_u32_e64 s[36:37], s29, v111
	s_nop 0
	s_and_b64 s[36:37], s[36:37], s[26:27]
	s_mov_b64 exec, s[36:37]
	ds_write_b32 v112, v113
	s_mov_b64 exec, -1
	v_add_u32_e32 v114, s28, v114
	s_cmp_lt_u32 s0, 5
	s_cbranch_scc1 .Ltk_p2_done
	v_cmp_eq_u32_e64 s[20:21], v200, v110
	v_cmp_eq_u32_e64 s[22:23], v201, v110
	v_cmp_eq_u32_e64 s[24:25], v202, v110
	v_cmp_eq_u32_e64 s[26:27], v203, v110
	s_bcnt1_i32_b64 s28, s[20:21]
	v_mbcnt_lo_u32_b32 v111, s20, v114
	v_mbcnt_hi_u32_b32 v111, s21, v111
	v_add_u32_e32 v113, 0x500, v109
	v_lshl_add_u32 v112, v111, 2, s89
	v_cmp_gt_u32_e64 s[36:37], s29, v111
	s_nop 0
	s_and_b64 s[36:37], s[36:37], s[20:21]
	s_mov_b64 exec, s[36:37]
	ds_write_b32 v112, v113
	s_mov_b64 exec, -1
	v_add_u32_e32 v114, s28, v114
	s_bcnt1_i32_b64 s28, s[22:23]
	v_mbcnt_lo_u32_b32 v111, s22, v114
	v_mbcnt_hi_u32_b32 v111, s23, v111
	v_add_u32_e32 v113, 0x501, v109
	v_lshl_add_u32 v112, v111, 2, s89
	v_cmp_gt_u32_e64 s[36:37], s29, v111
	s_nop 0
	s_and_b64 s[36:37], s[36:37], s[22:23]
	s_mov_b64 exec, s[36:37]
	ds_write_b32 v112, v113
	s_mov_b64 exec, -1
	v_add_u32_e32 v114, s28, v114
	s_bcnt1_i32_b64 s28, s[24:25]
	v_mbcnt_lo_u32_b32 v111, s24, v114
	v_mbcnt_hi_u32_b32 v111, s25, v111
	v_add_u32_e32 v113, 0x502, v109
	v_lshl_add_u32 v112, v111, 2, s89
	v_cmp_gt_u32_e64 s[36:37], s29, v111
	s_nop 0
	s_and_b64 s[36:37], s[36:37], s[24:25]
	s_mov_b64 exec, s[36:37]
	ds_write_b32 v112, v113
	s_mov_b64 exec, -1
	v_add_u32_e32 v114, s28, v114
	s_bcnt1_i32_b64 s28, s[26:27]
	v_mbcnt_lo_u32_b32 v111, s26, v114
	v_mbcnt_hi_u32_b32 v111, s27, v111
	v_add_u32_e32 v113, 0x503, v109
	v_lshl_add_u32 v112, v111, 2, s89
	v_cmp_gt_u32_e64 s[36:37], s29, v111
	s_nop 0
	s_and_b64 s[36:37], s[36:37], s[26:27]
	s_mov_b64 exec, s[36:37]
	ds_write_b32 v112, v113
	s_mov_b64 exec, -1
	v_add_u32_e32 v114, s28, v114
	s_cmp_lt_u32 s0, 6
	s_cbranch_scc1 .Ltk_p2_done
	v_cmp_eq_u32_e64 s[20:21], v204, v110
	v_cmp_eq_u32_e64 s[22:23], v205, v110
	v_cmp_eq_u32_e64 s[24:25], v206, v110
	v_cmp_eq_u32_e64 s[26:27], v207, v110
	s_bcnt1_i32_b64 s28, s[20:21]
	v_mbcnt_lo_u32_b32 v111, s20, v114
	v_mbcnt_hi_u32_b32 v111, s21, v111
	v_add_u32_e32 v113, 0x600, v109
	v_lshl_add_u32 v112, v111, 2, s89
	v_cmp_gt_u32_e64 s[36:37], s29, v111
	s_nop 0
	s_and_b64 s[36:37], s[36:37], s[20:21]
	s_mov_b64 exec, s[36:37]
	ds_write_b32 v112, v113
	s_mov_b64 exec, -1
	v_add_u32_e32 v114, s28, v114
	s_bcnt1_i32_b64 s28, s[22:23]
	v_mbcnt_lo_u32_b32 v111, s22, v114
	v_mbcnt_hi_u32_b32 v111, s23, v111
	v_add_u32_e32 v113, 0x601, v109
	v_lshl_add_u32 v112, v111, 2, s89
	v_cmp_gt_u32_e64 s[36:37], s29, v111
	s_nop 0
	s_and_b64 s[36:37], s[36:37], s[22:23]
	s_mov_b64 exec, s[36:37]
	ds_write_b32 v112, v113
	s_mov_b64 exec, -1
	v_add_u32_e32 v114, s28, v114
	s_bcnt1_i32_b64 s28, s[24:25]
	v_mbcnt_lo_u32_b32 v111, s24, v114
	v_mbcnt_hi_u32_b32 v111, s25, v111
	v_add_u32_e32 v113, 0x602, v109
	v_lshl_add_u32 v112, v111, 2, s89
	v_cmp_gt_u32_e64 s[36:37], s29, v111
	s_nop 0
	s_and_b64 s[36:37], s[36:37], s[24:25]
	s_mov_b64 exec, s[36:37]
	ds_write_b32 v112, v113
	s_mov_b64 exec, -1
	v_add_u32_e32 v114, s28, v114
	s_bcnt1_i32_b64 s28, s[26:27]
	v_mbcnt_lo_u32_b32 v111, s26, v114
	v_mbcnt_hi_u32_b32 v111, s27, v111
	v_add_u32_e32 v113, 0x603, v109
	v_lshl_add_u32 v112, v111, 2, s89
	v_cmp_gt_u32_e64 s[36:37], s29, v111
	s_nop 0
	s_and_b64 s[36:37], s[36:37], s[26:27]
	s_mov_b64 exec, s[36:37]
	ds_write_b32 v112, v113
	s_mov_b64 exec, -1
	v_add_u32_e32 v114, s28, v114
	s_cmp_lt_u32 s0, 7
	s_cbranch_scc1 .Ltk_p2_done
	v_cmp_eq_u32_e64 s[20:21], v208, v110
	v_cmp_eq_u32_e64 s[22:23], v209, v110
	v_cmp_eq_u32_e64 s[24:25], v210, v110
	v_cmp_eq_u32_e64 s[26:27], v211, v110
	s_bcnt1_i32_b64 s28, s[20:21]
	v_mbcnt_lo_u32_b32 v111, s20, v114
	v_mbcnt_hi_u32_b32 v111, s21, v111
	v_add_u32_e32 v113, 0x700, v109
	v_lshl_add_u32 v112, v111, 2, s89
	v_cmp_gt_u32_e64 s[36:37], s29, v111
	s_nop 0
	s_and_b64 s[36:37], s[36:37], s[20:21]
	s_mov_b64 exec, s[36:37]
	ds_write_b32 v112, v113
	s_mov_b64 exec, -1
	v_add_u32_e32 v114, s28, v114
	s_bcnt1_i32_b64 s28, s[22:23]
	v_mbcnt_lo_u32_b32 v111, s22, v114
	v_mbcnt_hi_u32_b32 v111, s23, v111
	v_add_u32_e32 v113, 0x701, v109
	v_lshl_add_u32 v112, v111, 2, s89
	v_cmp_gt_u32_e64 s[36:37], s29, v111
	s_nop 0
	s_and_b64 s[36:37], s[36:37], s[22:23]
	s_mov_b64 exec, s[36:37]
	ds_write_b32 v112, v113
	s_mov_b64 exec, -1
	v_add_u32_e32 v114, s28, v114
	s_bcnt1_i32_b64 s28, s[24:25]
	v_mbcnt_lo_u32_b32 v111, s24, v114
	v_mbcnt_hi_u32_b32 v111, s25, v111
	v_add_u32_e32 v113, 0x702, v109
	v_lshl_add_u32 v112, v111, 2, s89
	v_cmp_gt_u32_e64 s[36:37], s29, v111
	s_nop 0
	s_and_b64 s[36:37], s[36:37], s[24:25]
	s_mov_b64 exec, s[36:37]
	ds_write_b32 v112, v113
	s_mov_b64 exec, -1
	v_add_u32_e32 v114, s28, v114
	s_bcnt1_i32_b64 s28, s[26:27]
	v_mbcnt_lo_u32_b32 v111, s26, v114
	v_mbcnt_hi_u32_b32 v111, s27, v111
	v_add_u32_e32 v113, 0x703, v109
	v_lshl_add_u32 v112, v111, 2, s89
	v_cmp_gt_u32_e64 s[36:37], s29, v111
	s_nop 0
	s_and_b64 s[36:37], s[36:37], s[26:27]
	s_mov_b64 exec, s[36:37]
	ds_write_b32 v112, v113
	s_mov_b64 exec, -1
	v_add_u32_e32 v114, s28, v114
	s_cmp_lt_u32 s0, 8
	s_cbranch_scc1 .Ltk_p2_done
	v_cmp_eq_u32_e64 s[20:21], v212, v110
	v_cmp_eq_u32_e64 s[22:23], v213, v110
	v_cmp_eq_u32_e64 s[24:25], v214, v110
	v_cmp_eq_u32_e64 s[26:27], v215, v110
	s_bcnt1_i32_b64 s28, s[20:21]
	v_mbcnt_lo_u32_b32 v111, s20, v114
	v_mbcnt_hi_u32_b32 v111, s21, v111
	v_add_u32_e32 v113, 0x800, v109
	v_lshl_add_u32 v112, v111, 2, s89
	v_cmp_gt_u32_e64 s[36:37], s29, v111
	s_nop 0
	s_and_b64 s[36:37], s[36:37], s[20:21]
	s_mov_b64 exec, s[36:37]
	ds_write_b32 v112, v113
	s_mov_b64 exec, -1
	v_add_u32_e32 v114, s28, v114
	s_bcnt1_i32_b64 s28, s[22:23]
	v_mbcnt_lo_u32_b32 v111, s22, v114
	v_mbcnt_hi_u32_b32 v111, s23, v111
	v_add_u32_e32 v113, 0x801, v109
	v_lshl_add_u32 v112, v111, 2, s89
	v_cmp_gt_u32_e64 s[36:37], s29, v111
	s_nop 0
	s_and_b64 s[36:37], s[36:37], s[22:23]
	s_mov_b64 exec, s[36:37]
	ds_write_b32 v112, v113
	s_mov_b64 exec, -1
	v_add_u32_e32 v114, s28, v114
	s_bcnt1_i32_b64 s28, s[24:25]
	v_mbcnt_lo_u32_b32 v111, s24, v114
	v_mbcnt_hi_u32_b32 v111, s25, v111
	v_add_u32_e32 v113, 0x802, v109
	v_lshl_add_u32 v112, v111, 2, s89
	v_cmp_gt_u32_e64 s[36:37], s29, v111
	s_nop 0
	s_and_b64 s[36:37], s[36:37], s[24:25]
	s_mov_b64 exec, s[36:37]
	ds_write_b32 v112, v113
	s_mov_b64 exec, -1
	v_add_u32_e32 v114, s28, v114
	s_bcnt1_i32_b64 s28, s[26:27]
	v_mbcnt_lo_u32_b32 v111, s26, v114
	v_mbcnt_hi_u32_b32 v111, s27, v111
	v_add_u32_e32 v113, 0x803, v109
	v_lshl_add_u32 v112, v111, 2, s89
	v_cmp_gt_u32_e64 s[36:37], s29, v111
	s_nop 0
	s_and_b64 s[36:37], s[36:37], s[26:27]
	s_mov_b64 exec, s[36:37]
	ds_write_b32 v112, v113
	s_mov_b64 exec, -1
	v_add_u32_e32 v114, s28, v114
	s_cmp_lt_u32 s0, 9
	s_cbranch_scc1 .Ltk_p2_done
	v_cmp_eq_u32_e64 s[20:21], v216, v110
	v_cmp_eq_u32_e64 s[22:23], v217, v110
	v_cmp_eq_u32_e64 s[24:25], v218, v110
	v_cmp_eq_u32_e64 s[26:27], v219, v110
	s_bcnt1_i32_b64 s28, s[20:21]
	v_mbcnt_lo_u32_b32 v111, s20, v114
	v_mbcnt_hi_u32_b32 v111, s21, v111
	v_add_u32_e32 v113, 0x900, v109
	v_lshl_add_u32 v112, v111, 2, s89
	v_cmp_gt_u32_e64 s[36:37], s29, v111
	s_nop 0
	s_and_b64 s[36:37], s[36:37], s[20:21]
	s_mov_b64 exec, s[36:37]
	ds_write_b32 v112, v113
	s_mov_b64 exec, -1
	v_add_u32_e32 v114, s28, v114
	s_bcnt1_i32_b64 s28, s[22:23]
	v_mbcnt_lo_u32_b32 v111, s22, v114
	v_mbcnt_hi_u32_b32 v111, s23, v111
	v_add_u32_e32 v113, 0x901, v109
	v_lshl_add_u32 v112, v111, 2, s89
	v_cmp_gt_u32_e64 s[36:37], s29, v111
	s_nop 0
	s_and_b64 s[36:37], s[36:37], s[22:23]
	s_mov_b64 exec, s[36:37]
	ds_write_b32 v112, v113
	s_mov_b64 exec, -1
	v_add_u32_e32 v114, s28, v114
	s_bcnt1_i32_b64 s28, s[24:25]
	v_mbcnt_lo_u32_b32 v111, s24, v114
	v_mbcnt_hi_u32_b32 v111, s25, v111
	v_add_u32_e32 v113, 0x902, v109
	v_lshl_add_u32 v112, v111, 2, s89
	v_cmp_gt_u32_e64 s[36:37], s29, v111
	s_nop 0
	s_and_b64 s[36:37], s[36:37], s[24:25]
	s_mov_b64 exec, s[36:37]
	ds_write_b32 v112, v113
	s_mov_b64 exec, -1
	v_add_u32_e32 v114, s28, v114
	s_bcnt1_i32_b64 s28, s[26:27]
	v_mbcnt_lo_u32_b32 v111, s26, v114
	v_mbcnt_hi_u32_b32 v111, s27, v111
	v_add_u32_e32 v113, 0x903, v109
	v_lshl_add_u32 v112, v111, 2, s89
	v_cmp_gt_u32_e64 s[36:37], s29, v111
	s_nop 0
	s_and_b64 s[36:37], s[36:37], s[26:27]
	s_mov_b64 exec, s[36:37]
	ds_write_b32 v112, v113
	s_mov_b64 exec, -1
	v_add_u32_e32 v114, s28, v114
	s_cmp_lt_u32 s0, 10
	s_cbranch_scc1 .Ltk_p2_done
	v_cmp_eq_u32_e64 s[20:21], v220, v110
	v_cmp_eq_u32_e64 s[22:23], v221, v110
	v_cmp_eq_u32_e64 s[24:25], v222, v110
	v_cmp_eq_u32_e64 s[26:27], v223, v110
	s_bcnt1_i32_b64 s28, s[20:21]
	v_mbcnt_lo_u32_b32 v111, s20, v114
	v_mbcnt_hi_u32_b32 v111, s21, v111
	v_add_u32_e32 v113, 0xa00, v109
	v_lshl_add_u32 v112, v111, 2, s89
	v_cmp_gt_u32_e64 s[36:37], s29, v111
	s_nop 0
	s_and_b64 s[36:37], s[36:37], s[20:21]
	s_mov_b64 exec, s[36:37]
	ds_write_b32 v112, v113
	s_mov_b64 exec, -1
	v_add_u32_e32 v114, s28, v114
	s_bcnt1_i32_b64 s28, s[22:23]
	v_mbcnt_lo_u32_b32 v111, s22, v114
	v_mbcnt_hi_u32_b32 v111, s23, v111
	v_add_u32_e32 v113, 0xa01, v109
	v_lshl_add_u32 v112, v111, 2, s89
	v_cmp_gt_u32_e64 s[36:37], s29, v111
	s_nop 0
	s_and_b64 s[36:37], s[36:37], s[22:23]
	s_mov_b64 exec, s[36:37]
	ds_write_b32 v112, v113
	s_mov_b64 exec, -1
	v_add_u32_e32 v114, s28, v114
	s_bcnt1_i32_b64 s28, s[24:25]
	v_mbcnt_lo_u32_b32 v111, s24, v114
	v_mbcnt_hi_u32_b32 v111, s25, v111
	v_add_u32_e32 v113, 0xa02, v109
	v_lshl_add_u32 v112, v111, 2, s89
	v_cmp_gt_u32_e64 s[36:37], s29, v111
	s_nop 0
	s_and_b64 s[36:37], s[36:37], s[24:25]
	s_mov_b64 exec, s[36:37]
	ds_write_b32 v112, v113
	s_mov_b64 exec, -1
	v_add_u32_e32 v114, s28, v114
	s_bcnt1_i32_b64 s28, s[26:27]
	v_mbcnt_lo_u32_b32 v111, s26, v114
	v_mbcnt_hi_u32_b32 v111, s27, v111
	v_add_u32_e32 v113, 0xa03, v109
	v_lshl_add_u32 v112, v111, 2, s89
	v_cmp_gt_u32_e64 s[36:37], s29, v111
	s_nop 0
	s_and_b64 s[36:37], s[36:37], s[26:27]
	s_mov_b64 exec, s[36:37]
	ds_write_b32 v112, v113
	s_mov_b64 exec, -1
	v_add_u32_e32 v114, s28, v114
	s_cmp_lt_u32 s0, 11
	s_cbranch_scc1 .Ltk_p2_done
	v_cmp_eq_u32_e64 s[20:21], v224, v110
	v_cmp_eq_u32_e64 s[22:23], v225, v110
	v_cmp_eq_u32_e64 s[24:25], v226, v110
	v_cmp_eq_u32_e64 s[26:27], v227, v110
	s_bcnt1_i32_b64 s28, s[20:21]
	v_mbcnt_lo_u32_b32 v111, s20, v114
	v_mbcnt_hi_u32_b32 v111, s21, v111
	v_add_u32_e32 v113, 0xb00, v109
	v_lshl_add_u32 v112, v111, 2, s89
	v_cmp_gt_u32_e64 s[36:37], s29, v111
	s_nop 0
	s_and_b64 s[36:37], s[36:37], s[20:21]
	s_mov_b64 exec, s[36:37]
	ds_write_b32 v112, v113
	s_mov_b64 exec, -1
	v_add_u32_e32 v114, s28, v114
	s_bcnt1_i32_b64 s28, s[22:23]
	v_mbcnt_lo_u32_b32 v111, s22, v114
	v_mbcnt_hi_u32_b32 v111, s23, v111
	v_add_u32_e32 v113, 0xb01, v109
	v_lshl_add_u32 v112, v111, 2, s89
	v_cmp_gt_u32_e64 s[36:37], s29, v111
	s_nop 0
	s_and_b64 s[36:37], s[36:37], s[22:23]
	s_mov_b64 exec, s[36:37]
	ds_write_b32 v112, v113
	s_mov_b64 exec, -1
	v_add_u32_e32 v114, s28, v114
	s_bcnt1_i32_b64 s28, s[24:25]
	v_mbcnt_lo_u32_b32 v111, s24, v114
	v_mbcnt_hi_u32_b32 v111, s25, v111
	v_add_u32_e32 v113, 0xb02, v109
	v_lshl_add_u32 v112, v111, 2, s89
	v_cmp_gt_u32_e64 s[36:37], s29, v111
	s_nop 0
	s_and_b64 s[36:37], s[36:37], s[24:25]
	s_mov_b64 exec, s[36:37]
	ds_write_b32 v112, v113
	s_mov_b64 exec, -1
	v_add_u32_e32 v114, s28, v114
	s_bcnt1_i32_b64 s28, s[26:27]
	v_mbcnt_lo_u32_b32 v111, s26, v114
	v_mbcnt_hi_u32_b32 v111, s27, v111
	v_add_u32_e32 v113, 0xb03, v109
	v_lshl_add_u32 v112, v111, 2, s89
	v_cmp_gt_u32_e64 s[36:37], s29, v111
	s_nop 0
	s_and_b64 s[36:37], s[36:37], s[26:27]
	s_mov_b64 exec, s[36:37]
	ds_write_b32 v112, v113
	s_mov_b64 exec, -1
	v_add_u32_e32 v114, s28, v114
	s_cmp_lt_u32 s0, 12
	s_cbranch_scc1 .Ltk_p2_done
	v_cmp_eq_u32_e64 s[20:21], v228, v110
	v_cmp_eq_u32_e64 s[22:23], v229, v110
	v_cmp_eq_u32_e64 s[24:25], v230, v110
	v_cmp_eq_u32_e64 s[26:27], v231, v110
	s_bcnt1_i32_b64 s28, s[20:21]
	v_mbcnt_lo_u32_b32 v111, s20, v114
	v_mbcnt_hi_u32_b32 v111, s21, v111
	v_add_u32_e32 v113, 0xc00, v109
	v_lshl_add_u32 v112, v111, 2, s89
	v_cmp_gt_u32_e64 s[36:37], s29, v111
	s_nop 0
	s_and_b64 s[36:37], s[36:37], s[20:21]
	s_mov_b64 exec, s[36:37]
	ds_write_b32 v112, v113
	s_mov_b64 exec, -1
	v_add_u32_e32 v114, s28, v114
	s_bcnt1_i32_b64 s28, s[22:23]
	v_mbcnt_lo_u32_b32 v111, s22, v114
	v_mbcnt_hi_u32_b32 v111, s23, v111
	v_add_u32_e32 v113, 0xc01, v109
	v_lshl_add_u32 v112, v111, 2, s89
	v_cmp_gt_u32_e64 s[36:37], s29, v111
	s_nop 0
	s_and_b64 s[36:37], s[36:37], s[22:23]
	s_mov_b64 exec, s[36:37]
	ds_write_b32 v112, v113
	s_mov_b64 exec, -1
	v_add_u32_e32 v114, s28, v114
	s_bcnt1_i32_b64 s28, s[24:25]
	v_mbcnt_lo_u32_b32 v111, s24, v114
	v_mbcnt_hi_u32_b32 v111, s25, v111
	v_add_u32_e32 v113, 0xc02, v109
	v_lshl_add_u32 v112, v111, 2, s89
	v_cmp_gt_u32_e64 s[36:37], s29, v111
	s_nop 0
	s_and_b64 s[36:37], s[36:37], s[24:25]
	s_mov_b64 exec, s[36:37]
	ds_write_b32 v112, v113
	s_mov_b64 exec, -1
	v_add_u32_e32 v114, s28, v114
	s_bcnt1_i32_b64 s28, s[26:27]
	v_mbcnt_lo_u32_b32 v111, s26, v114
	v_mbcnt_hi_u32_b32 v111, s27, v111
	v_add_u32_e32 v113, 0xc03, v109
	v_lshl_add_u32 v112, v111, 2, s89
	v_cmp_gt_u32_e64 s[36:37], s29, v111
	s_nop 0
	s_and_b64 s[36:37], s[36:37], s[26:27]
	s_mov_b64 exec, s[36:37]
	ds_write_b32 v112, v113
	s_mov_b64 exec, -1
	v_add_u32_e32 v114, s28, v114
	s_cmp_lt_u32 s0, 13
	s_cbranch_scc1 .Ltk_p2_done
	v_cmp_eq_u32_e64 s[20:21], v232, v110
	v_cmp_eq_u32_e64 s[22:23], v233, v110
	v_cmp_eq_u32_e64 s[24:25], v234, v110
	v_cmp_eq_u32_e64 s[26:27], v235, v110
	s_bcnt1_i32_b64 s28, s[20:21]
	v_mbcnt_lo_u32_b32 v111, s20, v114
	v_mbcnt_hi_u32_b32 v111, s21, v111
	v_add_u32_e32 v113, 0xd00, v109
	v_lshl_add_u32 v112, v111, 2, s89
	v_cmp_gt_u32_e64 s[36:37], s29, v111
	s_nop 0
	s_and_b64 s[36:37], s[36:37], s[20:21]
	s_mov_b64 exec, s[36:37]
	ds_write_b32 v112, v113
	s_mov_b64 exec, -1
	v_add_u32_e32 v114, s28, v114
	s_bcnt1_i32_b64 s28, s[22:23]
	v_mbcnt_lo_u32_b32 v111, s22, v114
	v_mbcnt_hi_u32_b32 v111, s23, v111
	v_add_u32_e32 v113, 0xd01, v109
	v_lshl_add_u32 v112, v111, 2, s89
	v_cmp_gt_u32_e64 s[36:37], s29, v111
	s_nop 0
	s_and_b64 s[36:37], s[36:37], s[22:23]
	s_mov_b64 exec, s[36:37]
	ds_write_b32 v112, v113
	s_mov_b64 exec, -1
	v_add_u32_e32 v114, s28, v114
	s_bcnt1_i32_b64 s28, s[24:25]
	v_mbcnt_lo_u32_b32 v111, s24, v114
	v_mbcnt_hi_u32_b32 v111, s25, v111
	v_add_u32_e32 v113, 0xd02, v109
	v_lshl_add_u32 v112, v111, 2, s89
	v_cmp_gt_u32_e64 s[36:37], s29, v111
	s_nop 0
	s_and_b64 s[36:37], s[36:37], s[24:25]
	s_mov_b64 exec, s[36:37]
	ds_write_b32 v112, v113
	s_mov_b64 exec, -1
	v_add_u32_e32 v114, s28, v114
	s_bcnt1_i32_b64 s28, s[26:27]
	v_mbcnt_lo_u32_b32 v111, s26, v114
	v_mbcnt_hi_u32_b32 v111, s27, v111
	v_add_u32_e32 v113, 0xd03, v109
	v_lshl_add_u32 v112, v111, 2, s89
	v_cmp_gt_u32_e64 s[36:37], s29, v111
	s_nop 0
	s_and_b64 s[36:37], s[36:37], s[26:27]
	s_mov_b64 exec, s[36:37]
	ds_write_b32 v112, v113
	s_mov_b64 exec, -1
	v_add_u32_e32 v114, s28, v114
	s_cmp_lt_u32 s0, 14
	s_cbranch_scc1 .Ltk_p2_done
	v_cmp_eq_u32_e64 s[20:21], v236, v110
	v_cmp_eq_u32_e64 s[22:23], v237, v110
	v_cmp_eq_u32_e64 s[24:25], v238, v110
	v_cmp_eq_u32_e64 s[26:27], v239, v110
	s_bcnt1_i32_b64 s28, s[20:21]
	v_mbcnt_lo_u32_b32 v111, s20, v114
	v_mbcnt_hi_u32_b32 v111, s21, v111
	v_add_u32_e32 v113, 0xe00, v109
	v_lshl_add_u32 v112, v111, 2, s89
	v_cmp_gt_u32_e64 s[36:37], s29, v111
	s_nop 0
	s_and_b64 s[36:37], s[36:37], s[20:21]
	s_mov_b64 exec, s[36:37]
	ds_write_b32 v112, v113
	s_mov_b64 exec, -1
	v_add_u32_e32 v114, s28, v114
	s_bcnt1_i32_b64 s28, s[22:23]
	v_mbcnt_lo_u32_b32 v111, s22, v114
	v_mbcnt_hi_u32_b32 v111, s23, v111
	v_add_u32_e32 v113, 0xe01, v109
	v_lshl_add_u32 v112, v111, 2, s89
	v_cmp_gt_u32_e64 s[36:37], s29, v111
	s_nop 0
	s_and_b64 s[36:37], s[36:37], s[22:23]
	s_mov_b64 exec, s[36:37]
	ds_write_b32 v112, v113
	s_mov_b64 exec, -1
	v_add_u32_e32 v114, s28, v114
	s_bcnt1_i32_b64 s28, s[24:25]
	v_mbcnt_lo_u32_b32 v111, s24, v114
	v_mbcnt_hi_u32_b32 v111, s25, v111
	v_add_u32_e32 v113, 0xe02, v109
	v_lshl_add_u32 v112, v111, 2, s89
	v_cmp_gt_u32_e64 s[36:37], s29, v111
	s_nop 0
	s_and_b64 s[36:37], s[36:37], s[24:25]
	s_mov_b64 exec, s[36:37]
	ds_write_b32 v112, v113
	s_mov_b64 exec, -1
	v_add_u32_e32 v114, s28, v114
	s_bcnt1_i32_b64 s28, s[26:27]
	v_mbcnt_lo_u32_b32 v111, s26, v114
	v_mbcnt_hi_u32_b32 v111, s27, v111
	v_add_u32_e32 v113, 0xe03, v109
	v_lshl_add_u32 v112, v111, 2, s89
	v_cmp_gt_u32_e64 s[36:37], s29, v111
	s_nop 0
	s_and_b64 s[36:37], s[36:37], s[26:27]
	s_mov_b64 exec, s[36:37]
	ds_write_b32 v112, v113
	s_mov_b64 exec, -1
	v_add_u32_e32 v114, s28, v114
	s_cmp_lt_u32 s0, 15
	s_cbranch_scc1 .Ltk_p2_done
	v_cmp_eq_u32_e64 s[20:21], v134, v110
	v_cmp_eq_u32_e64 s[22:23], v135, v110
	v_cmp_eq_u32_e64 s[24:25], v136, v110
	v_cmp_eq_u32_e64 s[26:27], v137, v110
	s_bcnt1_i32_b64 s28, s[20:21]
	v_mbcnt_lo_u32_b32 v111, s20, v114
	v_mbcnt_hi_u32_b32 v111, s21, v111
	v_add_u32_e32 v113, 0xf00, v109
	v_lshl_add_u32 v112, v111, 2, s89
	v_cmp_gt_u32_e64 s[36:37], s29, v111
	s_nop 0
	s_and_b64 s[36:37], s[36:37], s[20:21]
	s_mov_b64 exec, s[36:37]
	ds_write_b32 v112, v113
	s_mov_b64 exec, -1
	v_add_u32_e32 v114, s28, v114
	s_bcnt1_i32_b64 s28, s[22:23]
	v_mbcnt_lo_u32_b32 v111, s22, v114
	v_mbcnt_hi_u32_b32 v111, s23, v111
	v_add_u32_e32 v113, 0xf01, v109
	v_lshl_add_u32 v112, v111, 2, s89
	v_cmp_gt_u32_e64 s[36:37], s29, v111
	s_nop 0
	s_and_b64 s[36:37], s[36:37], s[22:23]
	s_mov_b64 exec, s[36:37]
	ds_write_b32 v112, v113
	s_mov_b64 exec, -1
	v_add_u32_e32 v114, s28, v114
	s_bcnt1_i32_b64 s28, s[24:25]
	v_mbcnt_lo_u32_b32 v111, s24, v114
	v_mbcnt_hi_u32_b32 v111, s25, v111
	v_add_u32_e32 v113, 0xf02, v109
	v_lshl_add_u32 v112, v111, 2, s89
	v_cmp_gt_u32_e64 s[36:37], s29, v111
	s_nop 0
	s_and_b64 s[36:37], s[36:37], s[24:25]
	s_mov_b64 exec, s[36:37]
	ds_write_b32 v112, v113
	s_mov_b64 exec, -1
	v_add_u32_e32 v114, s28, v114
	s_bcnt1_i32_b64 s28, s[26:27]
	v_mbcnt_lo_u32_b32 v111, s26, v114
	v_mbcnt_hi_u32_b32 v111, s27, v111
	v_add_u32_e32 v113, 0xf03, v109
	v_lshl_add_u32 v112, v111, 2, s89
	v_cmp_gt_u32_e64 s[36:37], s29, v111
	s_nop 0
	s_and_b64 s[36:37], s[36:37], s[26:27]
	s_mov_b64 exec, s[36:37]
	ds_write_b32 v112, v113
	s_mov_b64 exec, -1
	v_add_u32_e32 v114, s28, v114

.Lat_A_full:
	v_max3_f32 v92, v82, v83, v84
	v_max3_f32 v93, v85, v86, v87
	v_max3_f32 v92, v92, v88, v89
	v_max_f32_e32 v92, v92, v93
	v_mov_b32_e32 v93, v92
	s_nop 1
	v_permlane16_swap_b32_e32 v92, v93
	v_max_f32_e32 v92, v92, v93
	v_mov_b32_e32 v93, v92
	s_nop 1
	v_permlane32_swap_b32_e32 v92, v93
	v_max3_f32 v180, v181, v92, v93
	v_sub_f32_e32 v94, v181, v180
	v_sub_f32_e32 v82, v82, v180
	v_sub_f32_e32 v83, v83, v180
	v_sub_f32_e32 v84, v84, v180
	v_sub_f32_e32 v85, v85, v180
	v_sub_f32_e32 v86, v86, v180
	v_sub_f32_e32 v87, v87, v180
	v_sub_f32_e32 v88, v88, v180
	v_sub_f32_e32 v89, v89, v180
	v_exp_f32_e32 v94, v94
	v_exp_f32_e32 v82, v82
	v_exp_f32_e32 v83, v83
	v_exp_f32_e32 v84, v84
	v_exp_f32_e32 v85, v85
	v_exp_f32_e32 v86, v86
	v_exp_f32_e32 v87, v87
	v_exp_f32_e32 v88, v88
	v_exp_f32_e32 v89, v89
	v_add_f32_e32 v92, v82, v83
	v_add_f32_e32 v93, v84, v85
	v_add_f32_e32 v97, v86, v87
	v_add_f32_e32 v92, v92, v93
	v_add_f32_e32 v96, v88, v89
	v_add_f32_e32 v97, v97, v96
	v_add_f32_e32 v92, v92, v97
	v_mov_b32_e32 v93, v92
	v_mov_b32_e32 v181, v180
	v_cvt_pk_bf16_f32 v82, v82, v83
	v_cvt_pk_bf16_f32 v83, v84, v85
	v_permlane16_swap_b32_e32 v92, v93
	v_add_f32_e32 v92, v92, v93
	v_mov_b32_e32 v93, v92
	v_cvt_pk_bf16_f32 v84, v86, v87
	v_cvt_pk_bf16_f32 v85, v88, v89
	v_permlane32_swap_b32_e32 v92, v93
	v_add_f32_e32 v92, v92, v93
	v_fma_f32 v179, v179, v94, v92
	v_pk_mul_f32 v[2:3], v[2:3], v[94:95] op_sel_hi:[1,0]
	v_pk_mul_f32 v[4:5], v[4:5], v[94:95] op_sel_hi:[1,0]
	v_pk_mul_f32 v[6:7], v[6:7], v[94:95] op_sel_hi:[1,0]
	v_pk_mul_f32 v[8:9], v[8:9], v[94:95] op_sel_hi:[1,0]
	v_pk_mul_f32 v[10:11], v[10:11], v[94:95] op_sel_hi:[1,0]
	v_pk_mul_f32 v[12:13], v[12:13], v[94:95] op_sel_hi:[1,0]
	v_pk_mul_f32 v[14:15], v[14:15], v[94:95] op_sel_hi:[1,0]
	v_pk_mul_f32 v[16:17], v[16:17], v[94:95] op_sel_hi:[1,0]
	v_pk_mul_f32 v[18:19], v[18:19], v[94:95] op_sel_hi:[1,0]
	v_pk_mul_f32 v[20:21], v[20:21], v[94:95] op_sel_hi:[1,0]
	v_pk_mul_f32 v[22:23], v[22:23], v[94:95] op_sel_hi:[1,0]
	v_pk_mul_f32 v[24:25], v[24:25], v[94:95] op_sel_hi:[1,0]
	v_pk_mul_f32 v[26:27], v[26:27], v[94:95] op_sel_hi:[1,0]
	v_pk_mul_f32 v[28:29], v[28:29], v[94:95] op_sel_hi:[1,0]
	v_pk_mul_f32 v[30:31], v[30:31], v[94:95] op_sel_hi:[1,0]
	v_pk_mul_f32 v[32:33], v[32:33], v[94:95] op_sel_hi:[1,0]
	s_cmp_ge_u32 s23, 3
	s_cbranch_scc1 .Lat_A_v24
	s_cmp_eq_u32 s23, 2
	s_cbranch_scc1 .Lat_A_v16
	s_waitcnt vmcnt(0)
	s_branch .Lat_A_pv

.Lat_A_pv:
	ds_read_b64_tr_b16 v[86:87], v188
	ds_read_b64_tr_b16 v[88:89], v188 offset:4096
	ds_read_b64_tr_b16 v[244:245], v189
	ds_read_b64_tr_b16 v[246:247], v189 offset:4096
	s_waitcnt lgkmcnt(2)
	v_mfma_f32_16x16x32_bf16 v[2:5], v[86:89], v[82:85], v[2:5]
	ds_read_b64_tr_b16 v[86:87], v190
	ds_read_b64_tr_b16 v[88:89], v190 offset:4096
	s_waitcnt lgkmcnt(2)
	v_mfma_f32_16x16x32_bf16 v[6:9], v[244:247], v[82:85], v[6:9]
	ds_read_b64_tr_b16 v[244:245], v191
	ds_read_b64_tr_b16 v[246:247], v191 offset:4096
	s_waitcnt lgkmcnt(2)
	v_mfma_f32_16x16x32_bf16 v[10:13], v[86:89], v[82:85], v[10:13]
	ds_read_b64_tr_b16 v[86:87], v192
	ds_read_b64_tr_b16 v[88:89], v192 offset:4096
	s_waitcnt lgkmcnt(2)
	v_mfma_f32_16x16x32_bf16 v[14:17], v[244:247], v[82:85], v[14:17]
	ds_read_b64_tr_b16 v[244:245], v193
	ds_read_b64_tr_b16 v[246:247], v193 offset:4096
	s_waitcnt lgkmcnt(2)
	v_mfma_f32_16x16x32_bf16 v[18:21], v[86:89], v[82:85], v[18:21]
	ds_read_b64_tr_b16 v[86:87], v194
	ds_read_b64_tr_b16 v[88:89], v194 offset:4096
	s_waitcnt lgkmcnt(2)
	v_mfma_f32_16x16x32_bf16 v[22:25], v[244:247], v[82:85], v[22:25]
	ds_read_b64_tr_b16 v[244:245], v195
	ds_read_b64_tr_b16 v[246:247], v195 offset:4096
	s_waitcnt lgkmcnt(2)
	v_mfma_f32_16x16x32_bf16 v[30:33], v[86:89], v[82:85], v[30:33]
	s_waitcnt lgkmcnt(0)
	v_mfma_f32_16x16x32_bf16 v[26:29], v[244:247], v[82:85], v[26:29]
	s_cmp_ge_u32 s23, 3
	s_cbranch_scc0 .Lat_A_nov
	s_mov_b32 m0, s26
	v_mad_u32_u24 v108, v100, s35, v177
	global_load_lds_dwordx4 v108, s[6:7]
	s_add_u32 m0, s26, 1024
	v_mad_u32_u24 v108, v101, s35, v178
	global_load_lds_dwordx4 v108, s[6:7]
	s_add_u32 m0, s26, 2048
	v_mad_u32_u24 v108, v102, s35, v177
	global_load_lds_dwordx4 v108, s[6:7]
	s_add_u32 m0, s26, 3072
	v_mad_u32_u24 v108, v103, s35, v178
	global_load_lds_dwordx4 v108, s[6:7]
	s_add_u32 m0, s26, 4096
	v_mad_u32_u24 v108, v104, s35, v177
	global_load_lds_dwordx4 v108, s[6:7]
	s_add_u32 m0, s26, 5120
	v_mad_u32_u24 v108, v105, s35, v178
	global_load_lds_dwordx4 v108, s[6:7]
	s_add_u32 m0, s26, 6144
	v_mad_u32_u24 v108, v106, s35, v177
	global_load_lds_dwordx4 v108, s[6:7]
	s_add_u32 m0, s26, 7168
	v_mad_u32_u24 v108, v107, s35, v178
	global_load_lds_dwordx4 v108, s[6:7]

.Lat_B_pv:
	ds_read_b64_tr_b16 v[86:87], v196
	ds_read_b64_tr_b16 v[88:89], v196 offset:4096
	ds_read_b64_tr_b16 v[244:245], v197
	ds_read_b64_tr_b16 v[246:247], v197 offset:4096
	s_waitcnt lgkmcnt(2)
	v_mfma_f32_16x16x32_bf16 v[2:5], v[86:89], v[82:85], v[2:5]
	ds_read_b64_tr_b16 v[86:87], v198
	ds_read_b64_tr_b16 v[88:89], v198 offset:4096
	s_waitcnt lgkmcnt(2)
	v_mfma_f32_16x16x32_bf16 v[6:9], v[244:247], v[82:85], v[6:9]
	ds_read_b64_tr_b16 v[244:245], v199
	ds_read_b64_tr_b16 v[246:247], v199 offset:4096
	s_waitcnt lgkmcnt(2)
	v_mfma_f32_16x16x32_bf16 v[10:13], v[86:89], v[82:85], v[10:13]
	ds_read_b64_tr_b16 v[86:87], v200
	ds_read_b64_tr_b16 v[88:89], v200 offset:4096
	s_waitcnt lgkmcnt(2)
	v_mfma_f32_16x16x32_bf16 v[14:17], v[244:247], v[82:85], v[14:17]
	ds_read_b64_tr_b16 v[244:245], v201
	ds_read_b64_tr_b16 v[246:247], v201 offset:4096
	s_waitcnt lgkmcnt(2)
	v_mfma_f32_16x16x32_bf16 v[18:21], v[86:89], v[82:85], v[18:21]
	ds_read_b64_tr_b16 v[86:87], v202
	ds_read_b64_tr_b16 v[88:89], v202 offset:4096
	s_waitcnt lgkmcnt(2)
	v_mfma_f32_16x16x32_bf16 v[22:25], v[244:247], v[82:85], v[22:25]
	ds_read_b64_tr_b16 v[244:245], v203
	ds_read_b64_tr_b16 v[246:247], v203 offset:4096
	s_waitcnt lgkmcnt(2)
	v_mfma_f32_16x16x32_bf16 v[30:33], v[86:89], v[82:85], v[30:33]
	s_waitcnt lgkmcnt(0)
	v_mfma_f32_16x16x32_bf16 v[26:29], v[244:247], v[82:85], v[26:29]
	s_cmp_ge_u32 s23, 3
	s_cbranch_scc0 .Lat_B_nov
	s_mov_b32 m0, s27
	v_mad_u32_u24 v108, v100, s35, v177
	global_load_lds_dwordx4 v108, s[6:7]
	s_add_u32 m0, s27, 1024
	v_mad_u32_u24 v108, v101, s35, v178
	global_load_lds_dwordx4 v108, s[6:7]
	s_add_u32 m0, s27, 2048
	v_mad_u32_u24 v108, v102, s35, v177
	global_load_lds_dwordx4 v108, s[6:7]
	s_add_u32 m0, s27, 3072
	v_mad_u32_u24 v108, v103, s35, v178
	global_load_lds_dwordx4 v108, s[6:7]
	s_add_u32 m0, s27, 4096
	v_mad_u32_u24 v108, v104, s35, v177
	global_load_lds_dwordx4 v108, s[6:7]
	s_add_u32 m0, s27, 5120
	v_mad_u32_u24 v108, v105, s35, v178
	global_load_lds_dwordx4 v108, s[6:7]
	s_add_u32 m0, s27, 6144
	v_mad_u32_u24 v108, v106, s35, v177
	global_load_lds_dwordx4 v108, s[6:7]
	s_add_u32 m0, s27, 7168
	v_mad_u32_u24 v108, v107, s35, v178
	global_load_lds_dwordx4 v108, s[6:7]

.LBB0_1127:
	s_or_b64 exec, exec, s[0:1]
	s_add_i32 s20, s43, s40
	s_cmpk_gt_i32 s20, 0x1fff
	s_cbranch_scc1 .Lpf_skip
	s_lshr_b32 s21, s20, 2
	s_lshr_b32 s22, s20, 11
	s_xor_b32 s21, s22, s21
	s_xor_b32 s21, s21, s20
	s_bfe_u32 s22, s20, 0xb0001
	s_and_b32 s21, s21, 1
	s_xor_b32 s23, s22, 0xfff
	s_cmp_eq_u32 s21, 0
	s_cselect_b32 s24, s22, s23
	s_cmp_lt_u32 s24, 0x100
	s_cbranch_scc1 .Lpf_skip
	s_ashr_i32 s26, s20, 12
	s_lshl_b32 s26, s26, 12
	s_add_u32 s26, s26, s24
	s_mov_b32 s27, 0
	s_lshl_b64 s[26:27], s[26:27], 14
	s_add_u32 s26, s84, s26
	s_addc_u32 s27, s85, s27
	s_lshr_b32 s24, s24, 8
	v_lshlrev_b32_e32 v138, 4, v151
	global_load_dwordx4 v[180:183], v138, s[26:27]
	global_load_dwordx4 v[184:187], v138, s[26:27] offset:1024
	s_cmp_lt_u32 s24, 2
	s_cbranch_scc1 .Lpf_done
	global_load_dwordx4 v[188:191], v138, s[26:27] offset:2048
	s_cmp_lt_u32 s24, 3
	s_cbranch_scc1 .Lpf_done
	global_load_dwordx4 v[192:195], v138, s[26:27] offset:3072
	s_cmp_lt_u32 s24, 4
	s_cbranch_scc1 .Lpf_done
	s_add_u32 s26, s26, 0x1000
	s_addc_u32 s27, s27, 0
	global_load_dwordx4 v[196:199], v138, s[26:27]
	s_cmp_lt_u32 s24, 5
	s_cbranch_scc1 .Lpf_done
	global_load_dwordx4 v[200:203], v138, s[26:27] offset:1024
	s_cmp_lt_u32 s24, 6
	s_cbranch_scc1 .Lpf_done
	global_load_dwordx4 v[204:207], v138, s[26:27] offset:2048
	s_cmp_lt_u32 s24, 7
	s_cbranch_scc1 .Lpf_done
	global_load_dwordx4 v[208:211], v138, s[26:27] offset:3072
	s_cmp_lt_u32 s24, 8
	s_cbranch_scc1 .Lpf_done
	s_add_u32 s26, s26, 0x1000
	s_addc_u32 s27, s27, 0
	global_load_dwordx4 v[212:215], v138, s[26:27]
	s_cmp_lt_u32 s24, 9
	s_cbranch_scc1 .Lpf_done
	global_load_dwordx4 v[216:219], v138, s[26:27] offset:1024
	s_cmp_lt_u32 s24, 10
	s_cbranch_scc1 .Lpf_done
	global_load_dwordx4 v[220:223], v138, s[26:27] offset:2048
	s_cmp_lt_u32 s24, 11
	s_cbranch_scc1 .Lpf_done
	global_load_dwordx4 v[224:227], v138, s[26:27] offset:3072
	s_cmp_lt_u32 s24, 12
	s_cbranch_scc1 .Lpf_done
	s_add_u32 s26, s26, 0x1000
	s_addc_u32 s27, s27, 0
	global_load_dwordx4 v[228:231], v138, s[26:27]
	s_cmp_lt_u32 s24, 13
	s_cbranch_scc1 .Lpf_done
	global_load_dwordx4 v[232:235], v138, s[26:27] offset:1024
	s_cmp_lt_u32 s24, 14
	s_cbranch_scc1 .Lpf_done
	global_load_dwordx4 v[236:239], v138, s[26:27] offset:2048
	s_cmp_lt_u32 s24, 15
	s_cbranch_scc1 .Lpf_done
	global_load_dwordx4 v[134:137], v138, s[26:27] offset:3072
.Lpf_done:
	s_mov_b32 s98, 1
.Lpf_skip:
	v_ashrrev_i32_e32 v34, 2, v151
	s_lshl_b64 s[0:1], s[96:97], 6
	v_ashrrev_i32_e32 v35, 31, v34
	s_add_u32 s0, s72, s0
	s_addc_u32 s1, s73, s1
	v_lshlrev_b64 v[36:37], 2, v[34:35]
	v_lshl_add_u64 v[38:39], s[0:1], 0, v[36:37]
	s_add_u32 s0, s96, 0x2000
	s_addc_u32 s1, s97, 0
	s_lshl_b64 s[2:3], s[0:1], 6
	s_add_u32 s2, s72, s2
	s_addc_u32 s3, s73, s3
	s_add_u32 s4, s96, 0x4000
	s_addc_u32 s5, s97, 0
	v_lshl_add_u64 v[40:41], s[2:3], 0, v[36:37]
	s_lshl_b64 s[2:3], s[4:5], 6
	s_add_u32 s2, s72, s2
	s_addc_u32 s3, s73, s3
	v_lshl_add_u64 v[36:37], s[2:3], 0, v[36:37]
	global_load_dword v43, v[38:39], off
	global_load_dword v69, v[40:41], off
	global_load_dword v70, v[36:37], off
	v_div_scale_f32 v46, s[2:3], v179, v179, 1.0
	v_rcp_f32_e32 v47, v46
	s_lshl_b64 s[2:3], s[96:97], 12
	s_add_u32 s6, s86, s2
	v_lshlrev_b32_e32 v44, 7, v34
	v_fma_f32 v35, -v46, v47, 1.0
	v_fmac_f32_e32 v47, v35, v47
	v_lshlrev_b32_e32 v35, 5, v151
	s_addc_u32 s7, s87, s3
	v_ashrrev_i32_e32 v45, 31, v44
	s_lshl_b64 s[0:1], s[0:1], 12
	v_and_b32_e32 v42, 0x60, v35
	v_lshlrev_b64 v[34:35], 1, v[44:45]
	s_add_u32 s0, s86, s0
	v_lshl_add_u64 v[36:37], s[6:7], 0, v[34:35]
	v_lshlrev_b32_e32 v146, 1, v42
	s_addc_u32 s1, s87, s1
	v_div_scale_f32 v48, vcc, 1.0, v179, 1.0
	s_waitcnt vmcnt(5)
	v_lshl_add_u64 v[62:63], v[36:37], 0, v[146:147]
	v_lshl_add_u64 v[36:37], s[0:1], 0, v[34:35]
	s_lshl_b64 s[0:1], s[4:5], 12
	v_mul_f32_e32 v49, v48, v47
	s_add_u32 s0, s86, s0
	s_waitcnt vmcnt(4)
	v_fma_f32 v50, -v46, v49, v48
	s_addc_u32 s1, s87, s1
	v_fmac_f32_e32 v49, v50, v47
	v_lshl_add_u64 v[34:35], s[0:1], 0, v[34:35]
	v_fma_f32 v46, -v46, v49, v48
	v_lshl_add_u64 v[64:65], v[36:37], 0, v[146:147]
	v_lshl_add_u64 v[66:67], v[34:35], 0, v[146:147]
	global_load_dwordx4 v[74:77], v[62:63], off
	global_load_dwordx4 v[34:37], v[62:63], off offset:48
	global_load_dwordx4 v[78:81], v[64:65], off
	global_load_dwordx4 v[38:41], v[64:65], off offset:48
	global_load_dwordx4 v[82:85], v[66:67], off
	v_div_fmas_f32 v46, v46, v47, v49
	v_div_fixup_f32 v68, v46, v179, 1.0
	global_load_dwordx4 v[86:89], v[62:63], off offset:32
	global_load_dwordx4 v[90:93], v[62:63], off offset:16
	global_load_dwordx4 v[94:97], v[64:65], off offset:32
	global_load_dwordx4 v[98:101], v[64:65], off offset:16
	global_load_dwordx4 v[102:105], v[66:67], off offset:32
	global_load_dwordx4 v[106:109], v[66:67], off offset:16
	s_waitcnt vmcnt(12)
	v_pk_mul_f32 v[58:59], v[4:5], v[68:69] op_sel_hi:[1,0]
	v_pk_mul_f32 v[54:55], v[8:9], v[68:69] op_sel_hi:[1,0]
	v_pk_mul_f32 v[60:61], v[2:3], v[68:69] op_sel_hi:[1,0]
	v_max_f32_e64 v2, |v58|, |v59|
	v_pk_mul_f32 v[56:57], v[6:7], v[68:69] op_sel_hi:[1,0]
	v_max_f32_e64 v3, |v54|, |v55|
	v_max3_f32 v2, |v60|, |v61|, v2
	v_max3_f32 v3, |v56|, |v57|, v3
	v_pk_mul_f32 v[50:51], v[12:13], v[68:69] op_sel_hi:[1,0]
	v_pk_mul_f32 v[46:47], v[16:17], v[68:69] op_sel_hi:[1,0]
	v_max3_f32 v2, v2, 0, v3
	v_pk_mul_f32 v[52:53], v[10:11], v[68:69] op_sel_hi:[1,0]
	v_max_f32_e64 v3, |v50|, |v51|
	v_pk_mul_f32 v[48:49], v[14:15], v[68:69] op_sel_hi:[1,0]
	v_max_f32_e64 v4, |v46|, |v47|
	v_max3_f32 v3, |v52|, |v53|, v3
	v_max3_f32 v4, |v48|, |v49|, v4
	v_pk_mul_f32 v[20:21], v[20:21], v[68:69] op_sel_hi:[1,0]
	v_pk_mul_f32 v[14:15], v[24:25], v[68:69] op_sel_hi:[1,0]
	v_max3_f32 v2, v2, v3, v4
	v_pk_mul_f32 v[18:19], v[18:19], v[68:69] op_sel_hi:[1,0]
	v_max_f32_e64 v3, |v20|, |v21|
	v_pk_mul_f32 v[16:17], v[22:23], v[68:69] op_sel_hi:[1,0]
	v_max_f32_e64 v4, |v14|, |v15|
	v_max3_f32 v3, |v18|, |v19|, v3
	v_max3_f32 v4, |v16|, |v17|, v4
	v_max3_f32 v2, v2, v3, v4
	s_waitcnt vmcnt(11)
	v_max3_f32 v4, v43, v69, v70
	v_sub_f32_e32 v5, v43, v4
	v_exp_f32_e32 v110, v5
	v_sub_f32_e32 v5, v69, v4
	v_exp_f32_e32 v5, v5
	v_sub_f32_e32 v4, v70, v4
	v_exp_f32_e32 v111, v4
	v_pk_mul_f32 v[10:11], v[32:33], v[68:69] op_sel_hi:[1,0]
	v_add_f32_e32 v4, v110, v5
	v_pk_mul_f32 v[6:7], v[28:29], v[68:69] op_sel_hi:[1,0]
	v_add_f32_e32 v4, v111, v4
	v_div_scale_f32 v22, s[0:1], v4, v4, 1.0
	v_rcp_f32_e32 v23, v22
	v_pk_mul_f32 v[12:13], v[30:31], v[68:69] op_sel_hi:[1,0]
	v_max_f32_e64 v3, |v10|, |v11|
	v_pk_mul_f32 v[8:9], v[26:27], v[68:69] op_sel_hi:[1,0]
	v_max_f32_e64 v24, |v6|, |v7|
	v_max3_f32 v3, |v12|, |v13|, v3
	v_max3_f32 v24, |v8|, |v9|, v24
	v_max3_f32 v43, v2, v3, v24
	v_fma_f32 v2, -v22, v23, 1.0
	v_fmac_f32_e32 v23, v2, v23
	v_div_scale_f32 v2, vcc, 1.0, v4, 1.0
	v_mul_f32_e32 v3, v2, v23
	v_fma_f32 v24, -v22, v3, v2
	v_fmac_f32_e32 v3, v24, v23
	v_fma_f32 v2, -v22, v3, v2
	v_div_fmas_f32 v2, v2, v23, v3
	v_div_fixup_f32 v112, v2, v4, 1.0
	v_mul_f32_e32 v113, v5, v112
	global_load_dwordx4 v[2:5], v[66:67], off offset:48
	s_waitcnt vmcnt(9)
	v_lshlrev_b32_e32 v22, 16, v78
	v_mul_f32_e32 v62, v113, v22
	v_and_b32_e32 v22, 0xffff0000, v78
	v_mul_f32_e32 v67, v113, v22
	v_lshlrev_b32_e32 v22, 16, v79
	v_mul_f32_e32 v71, v113, v22
	v_and_b32_e32 v22, 0xffff0000, v79
	s_waitcnt vmcnt(7)
	v_lshlrev_b32_e32 v115, 16, v82
	v_and_b32_e32 v78, 0xffff0000, v82
	v_lshlrev_b32_e32 v82, 16, v75
	v_and_b32_e32 v118, 0xffff0000, v75
	v_mul_f32_e32 v75, v113, v22
	v_lshlrev_b32_e32 v22, 16, v80
	v_mul_f32_e32 v32, v113, v22
	v_and_b32_e32 v22, 0xffff0000, v80
	v_mul_f32_e32 v66, v113, v22
	v_lshlrev_b32_e32 v22, 16, v81
	v_mul_f32_e32 v70, v113, v22
	v_and_b32_e32 v22, 0xffff0000, v81
	v_lshlrev_b32_e32 v114, 16, v74
	v_and_b32_e32 v116, 0xffff0000, v74
	v_mul_f32_e32 v74, v113, v22
	s_waitcnt vmcnt(3)
	v_lshlrev_b32_e32 v22, 16, v98
	v_mul_f32_e32 v31, v113, v22
	v_and_b32_e32 v22, 0xffff0000, v98
	v_mul_f32_e32 v65, v113, v22
	v_lshlrev_b32_e32 v22, 16, v99
	v_mul_f32_e32 v69, v113, v22
	v_and_b32_e32 v22, 0xffff0000, v99
	v_mul_f32_e32 v73, v113, v22
	v_lshlrev_b32_e32 v22, 16, v100
	v_mul_f32_e32 v29, v113, v22
	v_and_b32_e32 v22, 0xffff0000, v100
	v_mul_f32_e32 v63, v113, v22
	v_lshlrev_b32_e32 v22, 16, v101
	v_mul_f32_e32 v68, v113, v22
	v_and_b32_e32 v22, 0xffff0000, v101
	v_mul_f32_e32 v72, v113, v22
	v_lshlrev_b32_e32 v22, 16, v94
	v_mul_f32_e32 v24, v113, v22
	v_and_b32_e32 v22, 0xffff0000, v94
	v_mul_f32_e32 v27, v113, v22
	v_lshlrev_b32_e32 v22, 16, v95
	v_mul_f32_e32 v30, v113, v22
	v_and_b32_e32 v22, 0xffff0000, v95
	v_mul_f32_e32 v64, v113, v22
	v_lshlrev_b32_e32 v22, 16, v96
	v_mul_f32_e32 v23, v113, v22
	v_and_b32_e32 v22, 0xffff0000, v96
	v_mul_f32_e32 v26, v113, v22
	v_lshlrev_b32_e32 v22, 16, v97
	v_mul_f32_e32 v28, v113, v22
	v_and_b32_e32 v22, 0xffff0000, v97
	v_mul_f32_e32 v33, v113, v22
	v_lshlrev_b32_e32 v22, 16, v38
	v_and_b32_e32 v25, 0xffff0000, v38
	v_lshlrev_b32_e32 v130, 16, v39
	v_and_b32_e32 v131, 0xffff0000, v39
	v_pk_mul_f32 v[38:39], v[110:111], v[112:113] op_sel_hi:[1,0]
	v_lshlrev_b32_e32 v117, 16, v83
	v_and_b32_e32 v79, 0xffff0000, v83
	v_lshlrev_b32_e32 v83, 16, v76
	v_lshlrev_b32_e32 v119, 16, v84
	v_and_b32_e32 v76, 0xffff0000, v76
	v_and_b32_e32 v80, 0xffff0000, v84
	v_lshlrev_b32_e32 v84, 16, v77
	v_and_b32_e32 v77, 0xffff0000, v77
	v_fmac_f32_e32 v62, v38, v114
	v_fmac_f32_e32 v67, v38, v116
	v_fmac_f32_e32 v71, v38, v82
	v_fmac_f32_e32 v75, v38, v118
	v_lshlrev_b32_e32 v120, 16, v85
	v_and_b32_e32 v81, 0xffff0000, v85
	v_lshlrev_b32_e32 v85, 16, v90
	s_waitcnt vmcnt(1)
	v_lshlrev_b32_e32 v121, 16, v106
	v_and_b32_e32 v90, 0xffff0000, v90
	v_and_b32_e32 v98, 0xffff0000, v106
	v_lshlrev_b32_e32 v106, 16, v91
	v_and_b32_e32 v91, 0xffff0000, v91
	v_fmac_f32_e32 v62, v39, v115
	v_fmac_f32_e32 v67, v39, v78
	v_fmac_f32_e32 v71, v39, v117
	v_fmac_f32_e32 v75, v39, v79
	v_fmac_f32_e32 v32, v38, v83
	v_fmac_f32_e32 v66, v38, v76
	v_fmac_f32_e32 v70, v38, v84
	v_fmac_f32_e32 v74, v38, v77
	v_lshlrev_b32_e32 v122, 16, v107
	v_and_b32_e32 v99, 0xffff0000, v107
	v_lshlrev_b32_e32 v107, 16, v92
	v_lshlrev_b32_e32 v123, 16, v108
	v_and_b32_e32 v92, 0xffff0000, v92
	v_and_b32_e32 v100, 0xffff0000, v108
	v_lshlrev_b32_e32 v108, 16, v93
	v_and_b32_e32 v93, 0xffff0000, v93
	v_max_f32_e64 v78, |v62|, |v67|
	v_max_f32_e64 v79, |v71|, |v75|
	v_fmac_f32_e32 v32, v39, v119
	v_fmac_f32_e32 v66, v39, v80
	v_fmac_f32_e32 v70, v39, v120
	v_fmac_f32_e32 v74, v39, v81
	v_fmac_f32_e32 v31, v38, v85
	v_fmac_f32_e32 v65, v38, v90
	v_fmac_f32_e32 v69, v38, v106
	v_fmac_f32_e32 v73, v38, v91
	v_lshlrev_b32_e32 v124, 16, v109
	v_and_b32_e32 v101, 0xffff0000, v109
	v_lshlrev_b32_e32 v109, 16, v86
	v_lshlrev_b32_e32 v125, 16, v102
	v_and_b32_e32 v86, 0xffff0000, v86
	v_and_b32_e32 v94, 0xffff0000, v102
	v_lshlrev_b32_e32 v102, 16, v87
	v_and_b32_e32 v87, 0xffff0000, v87
	v_max3_f32 v43, v43, v78, v79
	v_max_f32_e64 v76, |v32|, |v66|
	v_max_f32_e64 v77, |v70|, |v74|
	v_fmac_f32_e32 v31, v39, v121
	v_fmac_f32_e32 v65, v39, v98
	v_fmac_f32_e32 v69, v39, v122
	v_fmac_f32_e32 v73, v39, v99
	v_fmac_f32_e32 v29, v38, v107
	v_fmac_f32_e32 v63, v38, v92
	v_fmac_f32_e32 v68, v38, v108
	v_fmac_f32_e32 v72, v38, v93
	v_lshlrev_b32_e32 v126, 16, v103
	v_and_b32_e32 v95, 0xffff0000, v103
	v_lshlrev_b32_e32 v103, 16, v88
	v_lshlrev_b32_e32 v127, 16, v104
	v_and_b32_e32 v88, 0xffff0000, v88
	v_and_b32_e32 v96, 0xffff0000, v104
	v_lshlrev_b32_e32 v104, 16, v89
	v_and_b32_e32 v89, 0xffff0000, v89
	v_max3_f32 v43, v43, v76, v77
	v_max_f32_e64 v76, |v31|, |v65|
	v_max_f32_e64 v77, |v69|, |v73|
	v_fmac_f32_e32 v29, v39, v123
	v_fmac_f32_e32 v63, v39, v100
	v_fmac_f32_e32 v68, v39, v124
	v_fmac_f32_e32 v72, v39, v101
	v_fmac_f32_e32 v24, v38, v109
	v_fmac_f32_e32 v27, v38, v86
	v_fmac_f32_e32 v30, v38, v102
	v_fmac_f32_e32 v64, v38, v87
	v_lshlrev_b32_e32 v128, 16, v105
	v_and_b32_e32 v97, 0xffff0000, v105
	v_max3_f32 v43, v43, v76, v77
	v_max_f32_e64 v76, |v29|, |v63|
	v_max_f32_e64 v77, |v68|, |v72|
	v_fmac_f32_e32 v24, v39, v125
	v_fmac_f32_e32 v27, v39, v94
	v_fmac_f32_e32 v30, v39, v126
	v_fmac_f32_e32 v64, v39, v95
	v_fmac_f32_e32 v23, v38, v103
	v_fmac_f32_e32 v26, v38, v88
	v_fmac_f32_e32 v28, v38, v104
	v_fmac_f32_e32 v33, v38, v89
	v_max3_f32 v43, v43, v76, v77
	v_max_f32_e64 v76, |v24|, |v27|
	v_max_f32_e64 v77, |v30|, |v64|
	v_fmac_f32_e32 v23, v39, v127
	v_fmac_f32_e32 v26, v39, v96
	v_fmac_f32_e32 v28, v39, v128
	v_fmac_f32_e32 v33, v39, v97
	v_max3_f32 v43, v43, v76, v77
	v_max_f32_e64 v76, |v23|, |v26|
	v_max_f32_e64 v77, |v28|, |v33|
	v_lshlrev_b32_e32 v105, 16, v34
	v_and_b32_e32 v34, 0xffff0000, v34
	v_mul_f32_e32 v25, v113, v25
	v_max3_f32 v43, v43, v76, v77
	s_waitcnt vmcnt(0)
	v_lshlrev_b32_e32 v77, 16, v3
	v_lshlrev_b32_e32 v76, 16, v35
	v_lshlrev_b32_e32 v129, 16, v2
	v_and_b32_e32 v2, 0xffff0000, v2
	v_fmac_f32_e32 v25, v38, v34
	v_pk_mul_f32 v[76:77], v[38:39], v[76:77]
	v_fmac_f32_e32 v25, v39, v2
	v_fma_f32 v2, v113, v130, v76
	v_add_f32_e32 v2, v2, v77
	v_and_b32_e32 v77, 0xffff0000, v3
	v_and_b32_e32 v76, 0xffff0000, v35
	v_mul_f32_e32 v22, v113, v22
	v_pk_mul_f32 v[34:35], v[38:39], v[76:77]
	v_fmac_f32_e32 v22, v38, v105
	v_fma_f32 v3, v113, v131, v34
	v_fmac_f32_e32 v22, v39, v129
	v_add_f32_e32 v34, v3, v35
	v_lshlrev_b32_e32 v77, 16, v4
	v_lshlrev_b32_e32 v76, 16, v36
	v_lshlrev_b32_e32 v132, 16, v40
	v_max_f32_e64 v78, |v22|, |v25|
	v_max_f32_e64 v3, |v2|, |v34|
	v_pk_mul_f32 v[76:77], v[38:39], v[76:77]
	v_max3_f32 v43, v43, v78, v3
	v_fma_f32 v3, v113, v132, v76
	v_add_f32_e32 v3, v3, v77
	v_and_b32_e32 v77, 0xffff0000, v4
	v_and_b32_e32 v76, 0xffff0000, v36
	v_and_b32_e32 v40, 0xffff0000, v40
	v_pk_mul_f32 v[76:77], v[38:39], v[76:77]
	v_lshlrev_b32_e32 v133, 16, v41
	v_fma_f32 v4, v113, v40, v76
	v_add_f32_e32 v4, v4, v77
	v_lshlrev_b32_e32 v77, 16, v5
	v_lshlrev_b32_e32 v76, 16, v37
	v_pk_mul_f32 v[76:77], v[38:39], v[76:77]
	v_and_b32_e32 v40, 0xffff0000, v37
	v_fma_f32 v35, v113, v133, v76
	v_and_b32_e32 v76, 0xffff0000, v41
	v_and_b32_e32 v41, 0xffff0000, v5
	v_pk_mul_f32 v[36:37], v[38:39], v[40:41]
	v_add_f32_e32 v35, v35, v77
	v_fma_f32 v5, v113, v76, v36
	v_add_f32_e32 v5, v5, v37
	v_max_f32_e64 v78, |v3|, |v4|
	v_max_f32_e64 v36, |v35|, |v5|
	v_max3_f32 v36, v43, v78, v36
	ds_bpermute_b32 v37, v163, v36
	v_cmp_eq_u32_e32 vcc, 0, v151
	s_waitcnt lgkmcnt(0)
	v_max_f32_e32 v37, v37, v37
	v_max_f32_e32 v36, v36, v37
	ds_bpermute_b32 v37, v164, v36
	s_waitcnt lgkmcnt(0)
	v_max_f32_e32 v37, v37, v37
	v_max_f32_e32 v36, v36, v37
	ds_bpermute_b32 v37, v165, v36
	s_waitcnt lgkmcnt(0)
	v_max_f32_e32 v37, v37, v37
	v_max_f32_e32 v36, v36, v37
	ds_bpermute_b32 v37, v166, v36
	s_waitcnt lgkmcnt(0)
	v_max_f32_e32 v37, v37, v37
	v_max_f32_e32 v36, v36, v37
	ds_bpermute_b32 v37, v161, v36
	s_waitcnt lgkmcnt(0)
	v_max_f32_e32 v37, v37, v37
	v_max_f32_e32 v36, v36, v37
	ds_bpermute_b32 v37, v162, v36
	s_waitcnt lgkmcnt(0)
	v_max_f32_e32 v37, v37, v37
	v_max_f32_e32 v36, v36, v37
	v_cmp_lt_f32_e64 s[0:1], 0, v36
	s_and_saveexec_b64 s[4:5], vcc
	s_cbranch_execz .LBB0_1129
	s_lshl_b64 s[6:7], s[96:97], 2
	v_readlane_b32 s8, v242, 39
	v_readlane_b32 s9, v242, 40
	s_add_u32 s6, s8, s6
	v_mul_f32_e32 v37, 0x3c010204, v36
	s_addc_u32 s7, s9, s7
	v_cndmask_b32_e64 v37, 1.0, v37, s[0:1]
	global_store_dword v147, v37, s[6:7]

	.amdhsa_kernel _Z10fwd_kernel4Args
		.amdhsa_group_segment_fixed_size 0
		.amdhsa_private_segment_fixed_size 0
		.amdhsa_kernarg_size 392
		.amdhsa_user_sgpr_count 2
		.amdhsa_user_sgpr_dispatch_ptr 0
		.amdhsa_user_sgpr_queue_ptr 0
		.amdhsa_user_sgpr_kernarg_segment_ptr 1
		.amdhsa_user_sgpr_dispatch_id 0
		.amdhsa_user_sgpr_kernarg_preload_length 0
		.amdhsa_user_sgpr_kernarg_preload_offset 0
		.amdhsa_user_sgpr_private_segment_size 0
		.amdhsa_uses_dynamic_stack 0
		.amdhsa_enable_private_segment 0
		.amdhsa_system_sgpr_workgroup_id_x 1
		.amdhsa_system_sgpr_workgroup_id_y 0
		.amdhsa_system_sgpr_workgroup_id_z 0
		.amdhsa_system_sgpr_workgroup_info 0
		.amdhsa_system_vgpr_workitem_id 0
		.amdhsa_next_free_vgpr 248
		.amdhsa_next_free_sgpr 100
		.amdhsa_accum_offset 248
		.amdhsa_reserve_vcc 1
		.amdhsa_float_round_mode_32 0
		.amdhsa_float_round_mode_16_64 0
		.amdhsa_float_denorm_mode_32 3
		.amdhsa_float_denorm_mode_16_64 3
		.amdhsa_dx10_clamp 1
		.amdhsa_ieee_mode 1
		.amdhsa_fp16_overflow 0
		.amdhsa_tg_split 0
		.amdhsa_exception_fp_ieee_invalid_op 0
		.amdhsa_exception_fp_denorm_src 0
		.amdhsa_exception_fp_ieee_div_zero 0
		.amdhsa_exception_fp_ieee_overflow 0
		.amdhsa_exception_fp_ieee_underflow 0
		.amdhsa_exception_fp_ieee_inexact 0
		.amdhsa_exception_int_div_zero 0
	.end_amdhsa_kernel

amdhsa.kernels:
  - .agpr_count:     0
    .args:
      - .offset:         0
        .size:           136
        .value_kind:     by_value
      - .offset:         136
        .size:           4
        .value_kind:     hidden_block_count_x
      - .offset:         140
        .size:           4
        .value_kind:     hidden_block_count_y
      - .offset:         144
        .size:           4
        .value_kind:     hidden_block_count_z
      - .offset:         148
        .size:           2
        .value_kind:     hidden_group_size_x
      - .offset:         150
        .size:           2
        .value_kind:     hidden_group_size_y
      - .offset:         152
        .size:           2
        .value_kind:     hidden_group_size_z
      - .offset:         154
        .size:           2
        .value_kind:     hidden_remainder_x
      - .offset:         156
        .size:           2
        .value_kind:     hidden_remainder_y
      - .offset:         158
        .size:           2
        .value_kind:     hidden_remainder_z
      - .offset:         176
        .size:           8
        .value_kind:     hidden_global_offset_x
      - .offset:         184
        .size:           8
        .value_kind:     hidden_global_offset_y
      - .offset:         192
        .size:           8
        .value_kind:     hidden_global_offset_z
      - .offset:         200
        .size:           2
        .value_kind:     hidden_grid_dims
      - .offset:         256
        .size:           4
        .value_kind:     hidden_dynamic_lds_size
    .group_segment_fixed_size: 0
    .kernarg_segment_align: 8
    .kernarg_segment_size: 392
    .language:       OpenCL C
    .language_version:
      - 2
      - 0
    .max_flat_workgroup_size: 512
    .name:           _Z10fwd_kernel4Args
    .private_segment_fixed_size: 0
    .sgpr_count:     106
    .sgpr_spill_count: 61
    .symbol:         _Z10fwd_kernel4Args.kd
    .uniform_work_group_size: 1
    .uses_dynamic_stack: false
    .vgpr_count:     248
    .vgpr_spill_count: 0
    .wavefront_size: 64
